# sa1: t1 + attention K/V staging loads addressed by a scalar tile base plus a per-lane 32-bit offset (64-bit VALU address arithmetic per tile removed)
# speedup vs baseline: 1.0004x; 1.0004x over previous
; __device__ __forceinline__ int v_st(int k, int c) { const int kk = (k & ~0xC) | ((k & 4) << 1) | ((k & 8) >> 1); return ((kk >> 3) * 4 + (c >> 5)) * 512 + ((kk & 7) * 32 + (c & 31)) * 2; }
; __device__ __forceinline__ int v_rd_base(int lane) { return ((lane & 3) << 3) | (((lane >> 2) & 3) << 6) | (((lane >> 4) & 1) << 5) | (((lane >> 5) & 1) << 8); }
; #define SLOAD(k0) do { vs0 = *reinterpret_cast<const bf16x8*>(&Vh[(size_t)((k0) + sr) * DM + sc]); vs1 = *reinterpret_cast<const bf16x8*>(&Vh[(size_t)((k0) + 32 + sr) * DM + sc]); \
;     ks = *reinterpret_cast<const bf16x8*>(&Kh[(size_t)((k0) + kr) * DM + kc]); } while (0)
; #define SWRITE(s) do { *(bf16x8*)(V_lds + (s) * SHM_V + vst0) = vs0; *(bf16x8*)(V_lds + (s) * SHM_V + vst1) = vs1; *(bf16x8*)(K_lds + (s) * SHM_K64 + kst) = ks; } while (0)
; __device__ __forceinline__ void diff_pass(const bf16_t* __restrict__ Qb, const bf16_t* __restrict__ Kh, const bf16_t* __restrict__ Vh, int seq, char* lds, f32x16 (&o)[4], const int wave_) {
;     ...
;     const bf16_t* Qw = Qb + (size_t)(wid * 32 + r32) * DM + hi * 8;
; #pragma unroll
;     for (int d0 = 0; d0 < 4; ++d0) qr[d0] = *reinterpret_cast<const bf16x8*>(Qw + d0 * 16);
;     const int sr = tid >> 4, sc = (tid & 15) * 8, vst0 = v_st(sr, sc), vst1 = v_st(32 + sr, sc);
;     const int kr = tid >> 3, kc = (tid & 7) * 8, kst = kswz<64>(kr, kc * 2);
;     const int vb0 = (int)(uintptr_t)V_lds + v_rd_base(lane);
;     bf16x8 vs0, vs1, ks;
;     ...
;     __syncthreads();
;     SLOAD(0); SWRITE(0); SLOAD(64); __syncthreads();
.LBB0_822:
	s_lshl_b32 s0, s36, 1
	s_mov_b32 s1, -1
	s_and_b32 s64, s0, 0x700
	s_ashr_i32 s0, s37, 6
	s_lshl_b32 s2, s37, 8
	v_mbcnt_lo_u32_b32 v0, s1, 0
	v_mbcnt_hi_u32_b32 v0, s1, v0
	s_ashr_i32 s1, s0, 31
	s_lshl_b64 s[6:7], s[0:1], 11
	s_and_b32 s2, s2, 0x700
	s_or_b32 s6, s6, s2
	s_lshl_b64 s[2:3], s[6:7], 11
	v_readlane_b32 s8, v252, 16
	v_readlane_b32 s9, v252, 17
	s_add_u32 s2, s8, s2
	s_addc_u32 s3, s9, s3
	s_lshl_b32 s8, s37, 4
	s_and_b32 s38, s8, 0x380
	s_lshl_b32 s8, s38, 1
	s_add_u32 s34, s2, s8
	s_addc_u32 s35, s3, 0
	s_lshl_b64 s[10:11], s[0:1], 22
	v_readlane_b32 s0, v251, 42
	s_add_u32 s0, s0, s10
	v_readlane_b32 s1, v251, 43
	s_addc_u32 s1, s1, s11
	s_add_u32 s28, s0, s8
	s_addc_u32 s29, s1, 0
	v_readlane_b32 s0, v251, 44
	s_add_u32 s0, s0, s10
	v_readlane_b32 s1, v251, 45
	s_addc_u32 s1, s1, s11
	v_or_b32_e32 v207, s55, v0
	s_add_u32 s30, s0, s8
	s_mov_b32 s0, -1
	s_addc_u32 s31, s1, 0
	v_mbcnt_lo_u32_b32 v0, s0, 0
	v_mbcnt_hi_u32_b32 v0, s0, v0
	v_or_b32_e32 v68, s55, v0
	s_movk_i32 s0, 0xffe0
	v_ashrrev_i32_e32 v0, 1, v68
	v_bfi_b32 v0, s0, v0, v68
	v_ashrrev_i32_e32 v1, 31, v0
	v_lshlrev_b64 v[0:1], 11, v[0:1]
	v_lshrrev_b32_e32 v2, 1, v68
	v_ashrrev_i32_e32 v12, 4, v68
	v_lshl_add_u64 v[0:1], s[34:35], 0, v[0:1]
	v_and_b32_e32 v160, 16, v2
	v_lshlrev_b32_e32 v24, 3, v68
	v_ashrrev_i32_e32 v13, 31, v12
	v_lshl_add_u64 v[0:1], v[0:1], 0, v[160:161]
	v_and_b32_e32 v2, 0x78, v24
	v_lshlrev_b64 v[48:49], 11, v[12:13]
	global_load_dwordx4 v[162:165], v[0:1], off
	global_load_dwordx4 v[166:169], v[0:1], off offset:32
	global_load_dwordx4 v[170:173], v[0:1], off offset:64
	global_load_dwordx4 v[174:177], v[0:1], off offset:96
	v_lshl_add_u64 v[0:1], s[30:31], 0, v[48:49]
	v_lshlrev_b32_e32 v4, 1, v2
	v_mov_b32_e32 v5, v161
	v_add_u32_e32 v14, 32, v12
	v_ashrrev_i32_e32 v16, 3, v68
	v_lshl_add_u64 v[18:19], v[0:1], 0, v[4:5]
	s_barrier
	global_load_dwordx4 v[0:3], v[18:19], off
	v_ashrrev_i32_e32 v15, 31, v14
	v_ashrrev_i32_e32 v17, 31, v16
	v_lshlrev_b32_e32 v64, 4, v68
	v_lshlrev_b64 v[6:7], 11, v[14:15]
	v_lshlrev_b64 v[50:51], 11, v[16:17]
	v_lshl_add_u64 v[6:7], s[30:31], 0, v[6:7]
	v_and_b32_e32 v20, 0x70, v64
	v_lshl_add_u64 v[8:9], s[28:29], 0, v[50:51]
	v_mov_b32_e32 v21, v161
	v_lshl_add_u64 v[4:5], v[6:7], 0, v[4:5]
	v_lshl_add_u64 v[22:23], v[8:9], 0, v[20:21]
	global_load_dwordx4 v[4:7], v[4:5], off
	v_and_b32_e32 v13, 0xfffff0, v12
	global_load_dwordx4 v[8:11], v[22:23], off
	v_add_co_u32_e32 v194, vcc, 0x20000, v18
	s_nop 1
	v_addc_co_u32_e32 v195, vcc, 0, v19, vcc
	global_load_dwordx4 v[52:55], v[194:195], off
	v_add_co_u32_e32 v194, vcc, 0x30000, v18
	s_nop 1
	v_addc_co_u32_e32 v195, vcc, 0, v19, vcc
	global_load_dwordx4 v[56:59], v[194:195], off
	v_add_co_u32_e32 v194, vcc, 0x20000, v22
	s_nop 1
	v_addc_co_u32_e32 v195, vcc, 0, v23, vcc
	global_load_dwordx4 v[60:63], v[194:195], off
	v_lshlrev_b32_e32 v15, 1, v12
	v_and_or_b32 v13, v15, 8, v13
	v_lshrrev_b32_e32 v15, 1, v12
	v_lshrrev_b32_e32 v13, 1, v13
	v_bfe_u32 v17, v24, 5, 2
	v_and_b32_e32 v12, 3, v12
	v_or_b32_e32 v13, v13, v17
	v_and_or_b32 v12, v15, 4, v12
	v_lshlrev_b32_e32 v13, 9, v13
	v_lshlrev_b32_e32 v12, 6, v12
	v_and_b32_e32 v15, 48, v64
	v_or3_b32 v218, v13, v12, v15
	v_and_b32_e32 v13, 0xfffff0, v14
	v_lshlrev_b32_e32 v14, 1, v14
	v_and_or_b32 v13, v14, 8, v13
	v_lshrrev_b32_e32 v13, 1, v13
	v_or_b32_e32 v13, v13, v17
	v_add_u32_e32 v70, 0, v218
	s_mov_b32 s0, 0x20000
	v_lshlrev_b32_e32 v13, 9, v13
	v_or3_b32 v219, v13, v12, v15
	v_lshlrev_b32_e32 v12, 7, v16
	v_and_b32_e32 v13, 0x70, v68
	s_mov_b32 s1, 0x30000
	v_bitop3_b32 v220, v20, v12, v13 bitop3:0xde
	v_add_u32_e32 v71, 0, v219
	v_add_u32_e32 v221, 0, v220
	v_and_b32_e32 v69, 31, v68
	v_lshlrev_b32_e32 v12, 7, v69
	v_and_b32_e32 v13, 0x70, v24
	v_bitop3_b32 v223, v160, v12, v13 bitop3:0xde
	v_add_u32_e32 v222, 0, v223
	s_add_i32 s39, 0, 0x12000
	v_and_b32_e32 v72, 63, v68
	s_mov_b32 s12, 0
	s_mov_b32 s13, s12
	s_mov_b32 s14, s12
	s_mov_b32 s15, s12
	s_mov_b32 s16, s12
	s_mov_b32 s17, s12
	s_mov_b32 s18, s12
	s_mov_b32 s19, s12
	s_mov_b32 s20, s12
	s_mov_b32 s21, s12
	s_mov_b32 s22, s12
	s_mov_b32 s23, s12
	s_mov_b32 s24, s12
	s_mov_b32 s25, s12
	s_mov_b32 s26, s12
	s_mov_b32 s27, s12
	s_cmp_lg_u32 0, -1
	s_mov_b32 s42, 1
	s_mov_b32 s40, -1
	s_mov_b32 s41, 2
	v_mov_b32_e32 v230, 1.0
	v_mov_b32_e32 v215, 0
	s_waitcnt vmcnt(5)
	ds_write_b128 v70, v[0:3]
	s_waitcnt vmcnt(4)
	ds_write_b128 v71, v[4:7]
	s_waitcnt vmcnt(3)
	ds_write_b128 v221, v[8:11] offset:49152
	v_and_b32_e32 v8, 0x3fffffc0, v68
	s_waitcnt lgkmcnt(0)
	s_barrier
	ds_read_b128 v[0:3], v222 offset:49152
	ds_read_b128 v[4:7], v222 offset:53248
	s_waitcnt lgkmcnt(1)
	v_mfma_f32_32x32x16_bf16 v[16:31], v[0:3], v[162:165], 0
	v_or_b32_e32 v0, 32, v160
	v_bitop3_b32 v226, v0, v12, v13 bitop3:0xde
	v_add_u32_e32 v224, 0, v226
	ds_read_b128 v[0:3], v224 offset:49152
	v_lshl_add_u32 v213, v8, 2, s39
	s_cselect_b32 s0, 0, 0
	v_lshl_add_u32 v214, v69, 2, v213
	s_waitcnt lgkmcnt(1)
	v_mfma_f32_32x32x16_bf16 v[32:47], v[4:7], v[162:165], 0
	ds_read_b128 v[4:7], v224 offset:53248
	s_waitcnt lgkmcnt(1)
	v_mfma_f32_32x32x16_bf16 v[16:31], v[0:3], v[166:169], v[16:31]
	v_or_b32_e32 v0, 64, v160
	v_bitop3_b32 v228, v0, v12, v13 bitop3:0xde
	v_add_u32_e32 v225, 0, v228
	ds_read_b128 v[0:3], v225 offset:53248
	ds_read_b128 v[8:11], v225 offset:49152
	s_waitcnt lgkmcnt(2)
	v_mfma_f32_32x32x16_bf16 v[32:47], v[4:7], v[166:169], v[32:47]
	v_lshlrev_b32_e32 v4, 3, v72
	v_and_b32_e32 v5, 0xc0, v64
	v_lshlrev_b32_e32 v6, 1, v68
	v_and_or_b32 v5, v4, 24, v5
	v_and_b32_e32 v6, 32, v6
	v_and_b32_e32 v4, 0x100, v4
	v_or3_b32 v216, v5, v6, v4
	s_waitcnt lgkmcnt(0)
	v_mfma_f32_32x32x16_bf16 v[16:31], v[8:11], v[170:173], v[16:31]
	v_or_b32_e32 v4, 0x60, v160
	v_bitop3_b32 v229, v4, v12, v13 bitop3:0xde
	v_add_u32_e32 v227, 0, v229
	ds_read_b128 v[64:67], v227 offset:53248
	ds_read_b128 v[4:7], v227 offset:49152
	s_waitcnt vmcnt(2)
	ds_write_b128 v70, v[52:55] offset:16384
	s_waitcnt vmcnt(1)
	ds_write_b128 v71, v[56:59] offset:16384
	s_waitcnt vmcnt(0)
	ds_write_b128 v221, v[60:63] offset:57344
	v_mfma_f32_32x32x16_bf16 v[32:47], v[0:3], v[170:173], v[32:47]
	v_add_u32_e32 v217, s0, v216
	v_cmp_gt_u32_e64 s[0:1], 32, v72
	s_waitcnt lgkmcnt(0)
	s_barrier
; #define SWRITE(s) do { *(bf16x8*)(V_lds + (s) * SHM_V + vst0) = vs0; *(bf16x8*)(V_lds + (s) * SHM_V + vst1) = vs1; *(bf16x8*)(K_lds + (s) * SHM_K64 + kst) = ks; } while (0)
; #define ROT() do { s_prev = s_cur; s_cur = s_next; s_next = (s_next == DA_NBUF - 1) ? 0 : s_next + 1; } while (0)
; #define EX2(x) x = __builtin_amdgcn_exp2f(x)
; __device__ __forceinline__ void diff_pass(const bf16_t* __restrict__ Qb, const bf16_t* __restrict__ Kh, const bf16_t* __restrict__ Vh, int seq, char* lds, f32x16 (&o)[4], const int wave_) {
;     ...
;     negm = f32x16{};
;     qkt64c(pA0, pA1, K_lds, qr, negm, r32, hi);
;     { const float pm = rowmax32(pA0, pA1); m_reg = pm; alA = 1.f;
; #pragma unroll
;       for (int r = 0; r < 16; ++r) { pA0[r] -= pm; pA1[r] -= pm; negm[r] = -pm; }
; #pragma unroll
;       for (int r = 0; r < 16; ++r) EX2(pA0[r]);
; #pragma unroll
;       for (int r = 0; r < 8; ++r) EX2(pA1[r]); }
;     SWRITE(1); __syncthreads();
;     ROT();
	v_mfma_f32_32x32x16_bf16 v[16:31], v[4:7], v[174:177], v[16:31]
	v_mov_b64_e32 v[0:1], s[12:13]
	v_mov_b64_e32 v[14:15], s[26:27]
	v_mov_b64_e32 v[2:3], s[14:15]
	v_mov_b64_e32 v[4:5], s[16:17]
	v_mov_b64_e32 v[6:7], s[18:19]
	v_mov_b64_e32 v[8:9], s[20:21]
	v_mov_b64_e32 v[10:11], s[22:23]
	v_mfma_f32_32x32x16_bf16 v[32:47], v[64:67], v[174:177], v[32:47]
	s_nop 3
	v_max_f32_e32 v64, v17, v17
	v_max_f32_e32 v65, v16, v16
	v_max_f32_e32 v64, v65, v64
	v_mov_b64_e32 v[12:13], s[24:25]
	s_nop 3
	v_max3_f32 v65, v18, v19, v33
	v_max3_f32 v64, v64, v32, v34
	v_max3_f32 v64, v64, v35, v20
	v_max3_f32 v65, v65, v22, v23
	v_max3_f32 v64, v64, v21, v36
	v_max3_f32 v65, v65, v38, v39
	v_max3_f32 v64, v64, v37, v24
	v_max3_f32 v65, v65, v26, v27
	v_max3_f32 v64, v64, v25, v40
	v_max3_f32 v65, v65, v42, v43
	v_max3_f32 v64, v64, v41, v28
	v_max3_f32 v65, v65, v30, v31
	v_max3_f32 v64, v64, v29, v44
	v_max3_f32 v65, v65, v46, v47
	v_max3_f32 v64, v64, v45, v65
	v_mov_b32_e32 v65, v64
	s_nop 1
	v_permlane32_swap_b32_e32 v64, v65
	v_max_f32_e32 v65, v65, v65
	v_max_f32_e32 v64, v64, v64
	v_max_f32_e32 v196, v64, v65
	v_sub_f32_e32 v16, v16, v196
	v_sub_f32_e32 v17, v17, v196
	v_sub_f32_e32 v18, v18, v196
	v_exp_f32_e32 v96, v16
	v_exp_f32_e32 v97, v17
	v_exp_f32_e32 v98, v18
	v_lshl_add_u64 v[16:17], s[10:11], 0, v[50:51]
	v_and_b32_e32 v18, 7, v68
	v_sub_f32_e32 v32, v32, v196
	v_sub_f32_e32 v33, v33, v196
	v_sub_f32_e32 v34, v34, v196
	v_sub_f32_e32 v19, v19, v196
	v_sub_f32_e32 v35, v35, v196
	v_sub_f32_e32 v20, v20, v196
	v_sub_f32_e32 v36, v36, v196
	v_sub_f32_e32 v21, v21, v196
	v_sub_f32_e32 v37, v37, v196
	v_sub_f32_e32 v22, v22, v196
	v_sub_f32_e32 v38, v38, v196
	v_sub_f32_e32 v23, v23, v196
	v_sub_f32_e32 v39, v39, v196
	v_sub_f32_e32 v24, v24, v196
	v_sub_f32_e32 v25, v25, v196
	v_sub_f32_e32 v26, v26, v196
	v_sub_f32_e32 v27, v27, v196
	v_sub_f32_e32 v28, v28, v196
	v_sub_f32_e32 v29, v29, v196
	v_sub_f32_e32 v30, v30, v196
	v_sub_f32_e32 v31, v31, v196
	v_lshl_or_b32 v16, v18, 4, v16
	v_exp_f32_e32 v99, v19
	v_exp_f32_e32 v100, v20
	v_exp_f32_e32 v101, v21
	v_exp_f32_e32 v102, v22
	v_exp_f32_e32 v103, v23
	v_exp_f32_e32 v104, v24
	v_exp_f32_e32 v105, v25
	v_exp_f32_e32 v106, v26
	v_exp_f32_e32 v107, v27
	v_exp_f32_e32 v108, v28
	v_exp_f32_e32 v109, v29
	v_exp_f32_e32 v110, v30
	v_exp_f32_e32 v111, v31
	v_exp_f32_e32 v112, v32
	v_exp_f32_e32 v113, v33
	v_exp_f32_e32 v114, v34
	v_exp_f32_e32 v115, v35
	v_exp_f32_e32 v116, v36
	v_exp_f32_e32 v117, v37
	v_exp_f32_e32 v118, v38
	v_exp_f32_e32 v119, v39
	v_lshl_add_u64 v[198:199], s[52:53], 0, v[16:17]
	v_lshl_add_u64 v[16:17], s[10:11], 0, v[48:49]
	v_and_b32_e32 v18, 15, v68
	v_lshl_or_b32 v16, v18, 4, v16
	v_xor_b32_e32 v80, 0x80000000, v196
	v_pk_add_f32 v[120:121], v[40:41], v[196:197] op_sel_hi:[1,0] neg_lo:[0,1] neg_hi:[0,1]
	v_pk_add_f32 v[122:123], v[42:43], v[196:197] op_sel_hi:[1,0] neg_lo:[0,1] neg_hi:[0,1]
	v_pk_add_f32 v[124:125], v[44:45], v[196:197] op_sel_hi:[1,0] neg_lo:[0,1] neg_hi:[0,1]
	v_pk_add_f32 v[126:127], v[46:47], v[196:197] op_sel_hi:[1,0] neg_lo:[0,1] neg_hi:[0,1]
	v_lshl_add_u64 v[200:201], s[52:53], 0, v[16:17]
	s_add_u32 s14, s52, s10
	s_addc_u32 s15, s53, s11
	s_add_u32 s14, s14, s64
	s_addc_u32 s15, s15, s65
	s_add_u32 s16, s14, 0x8a40000
	s_addc_u32 s17, s15, 0
	s_add_u32 s14, s14, 0x6a40000
	s_addc_u32 s15, s15, 0
	v_lshrrev_b32_e32 v194, 3, v207
	v_and_b32_e32 v195, 7, v207
	v_lshlrev_b32_e32 v194, 11, v194
	v_lshl_or_b32 v194, v195, 4, v194
	v_lshrrev_b32_e32 v195, 4, v207
	v_and_b32_e32 v255, 15, v207
	v_lshlrev_b32_e32 v195, 11, v195
	v_lshl_or_b32 v195, v255, 4, v195
	v_add_u32_e32 v255, 0x10000, v195
	v_mov_b64_e32 v[62:63], v[14:15]
	v_mov_b64_e32 v[46:47], v[14:15]
	v_mov_b64_e32 v[30:31], v[14:15]
	v_mov_b64_e32 v[60:61], v[12:13]
	v_mov_b64_e32 v[58:59], v[10:11]
	v_mov_b64_e32 v[56:57], v[8:9]
	v_mov_b64_e32 v[54:55], v[6:7]
	v_mov_b64_e32 v[52:53], v[4:5]
	v_mov_b64_e32 v[50:51], v[2:3]
	v_mov_b64_e32 v[48:49], v[0:1]
	v_mov_b64_e32 v[44:45], v[12:13]
	v_mov_b64_e32 v[42:43], v[10:11]
	v_mov_b64_e32 v[40:41], v[8:9]
	v_mov_b64_e32 v[38:39], v[6:7]
	v_mov_b64_e32 v[36:37], v[4:5]
	v_mov_b64_e32 v[34:35], v[2:3]
	v_mov_b64_e32 v[32:33], v[0:1]
	v_mov_b64_e32 v[28:29], v[12:13]
	v_mov_b64_e32 v[26:27], v[10:11]
	v_mov_b64_e32 v[24:25], v[8:9]
	v_mov_b64_e32 v[22:23], v[6:7]
	v_mov_b64_e32 v[20:21], v[4:5]
	v_mov_b64_e32 v[18:19], v[2:3]
	v_mov_b64_e32 v[16:17], v[0:1]
	v_mov_b32_e32 v81, v80
	v_mov_b32_e32 v82, v80
	v_mov_b32_e32 v83, v80
	v_mov_b32_e32 v84, v80
	v_mov_b32_e32 v85, v80
	v_mov_b32_e32 v86, v80
	v_mov_b32_e32 v87, v80
	v_mov_b32_e32 v88, v80
	v_mov_b32_e32 v89, v80
	v_mov_b32_e32 v90, v80
	v_mov_b32_e32 v91, v80
	v_mov_b32_e32 v92, v80
	v_mov_b32_e32 v93, v80
	v_mov_b32_e32 v94, v80
	v_mov_b32_e32 v95, v80

; #define SBAR() __builtin_amdgcn_sched_barrier(0)
; #define SLOAD(k0) do { vs0 = *reinterpret_cast<const bf16x8*>(&Vh[(size_t)((k0) + sr) * DM + sc]); vs1 = *reinterpret_cast<const bf16x8*>(&Vh[(size_t)((k0) + 32 + sr) * DM + sc]); \
;     ks = *reinterpret_cast<const bf16x8*>(&Kh[(size_t)((k0) + kr) * DM + kc]); } while (0)
; __device__ __forceinline__ void diff_pass(const bf16_t* __restrict__ Qb, const bf16_t* __restrict__ Kh, const bf16_t* __restrict__ Vh, int seq, char* lds, f32x16 (&o)[4], const int wave_) {
;     ...
;     for (int j = 1; j + 1 < NT; j += 2) {
;         SLOAD((j + 1) * 64);
;         SBAR(); qkt64c(pB0, pB1, K_lds + s_cur * SHM_K64, qr, negm, r32, hi); FIN(pA0, pA1, alA); SBAR();
;         YSEG(pB0, pB1, alB, s_prev);
.Latt9_p1_top:
	ds_read_b128 v[144:147], v128 offset:49152
	ds_read_b128 v[148:151], v129 offset:49152
	ds_read_b128 v[152:155], v130 offset:49152
	ds_read_b128 v[156:159], v131 offset:49152
	ds_read_b128 v[232:235], v128 offset:53248
	ds_read_b128 v[236:239], v129 offset:53248
	ds_read_b128 v[240:243], v130 offset:53248
	ds_read_b128 v[244:247], v131 offset:53248
	global_load_dwordx4 v[178:181], v195, s[16:17]
	global_load_dwordx4 v[182:185], v255, s[16:17]
	global_load_dwordx4 v[186:189], v194, s[14:15]
	s_add_u32 s16, s16, 0x20000
	s_addc_u32 s17, s17, 0
	s_add_u32 s14, s14, 0x20000
	s_addc_u32 s15, s15, 0
	v_exp_f32_e32 v190, v120
	v_exp_f32_e32 v191, v121
	v_add_f32_e32 v120, v96, v97
	v_add_f32_e32 v121, v98, v99
	s_waitcnt lgkmcnt(7)
	v_mfma_f32_32x32x16_bf16 v[128:143], v[144:147], v[162:165], v[80:95]
	v_exp_f32_e32 v192, v122
	v_add_f32_e32 v120, v120, v121
	v_add_f32_e32 v121, v100, v101
	v_add_f32_e32 v122, v102, v103
	v_exp_f32_e32 v193, v123
	s_waitcnt lgkmcnt(6)
	v_mfma_f32_32x32x16_bf16 v[128:143], v[148:151], v[166:169], v[128:143]
	v_add_f32_e32 v121, v121, v122
	v_add_f32_e32 v122, v104, v105
	v_add_f32_e32 v123, v106, v107
	v_add_f32_e32 v122, v122, v123
	v_add_f32_e32 v123, v108, v109
	s_waitcnt lgkmcnt(5)
	v_mfma_f32_32x32x16_bf16 v[128:143], v[152:155], v[170:173], v[128:143]
	v_add_f32_e32 v208, v110, v111
	v_add_f32_e32 v123, v123, v208
	v_add_f32_e32 v208, v112, v113
	v_add_f32_e32 v209, v114, v115
	v_add_f32_e32 v208, v208, v209
	s_waitcnt lgkmcnt(4)
	v_mfma_f32_32x32x16_bf16 v[128:143], v[156:159], v[174:177], v[128:143]
	v_exp_f32_e32 v124, v124
	v_exp_f32_e32 v125, v125
	s_waitcnt lgkmcnt(3)
	v_mfma_f32_32x32x16_bf16 v[144:159], v[232:235], v[162:165], v[80:95]
	v_lshl_add_u32 v234, s12, 14, v217
	ds_read_b64_tr_b16 v[64:65], v234 offset:0
	ds_read_b64_tr_b16 v[66:67], v234 offset:0x800
	ds_read_b64_tr_b16 v[68:69], v234 offset:0x1000
	ds_read_b64_tr_b16 v[70:71], v234 offset:0x1800
	ds_read_b64_tr_b16 v[72:73], v234 offset:0x2000
	ds_read_b64_tr_b16 v[74:75], v234 offset:0x2800
	ds_read_b64_tr_b16 v[76:77], v234 offset:0x3000
	ds_read_b64_tr_b16 v[78:79], v234 offset:0x3800
	v_exp_f32_e32 v126, v126
	v_exp_f32_e32 v127, v127
	v_add_f32_e32 v120, v208, v120
	v_add_f32_e32 v208, v116, v117
	v_add_f32_e32 v209, v118, v119
	v_add_f32_e32 v208, v208, v209
	v_add_f32_e32 v121, v208, v121
	s_waitcnt lgkmcnt(10)
	v_mfma_f32_32x32x16_bf16 v[144:159], v[236:239], v[166:169], v[144:159]
	v_add_f32_e32 v208, v190, v191
	v_add_f32_e32 v209, v192, v193
	v_add_f32_e32 v208, v208, v209
	v_add_f32_e32 v122, v122, v208
	v_add_f32_e32 v208, v124, v125
	v_add_f32_e32 v209, v126, v127
	v_add_f32_e32 v208, v208, v209
	s_waitcnt lgkmcnt(9)
	v_mfma_f32_32x32x16_bf16 v[144:159], v[240:243], v[170:173], v[144:159]
	v_add_f32_e32 v123, v123, v208
	v_add_f32_e32 v120, v120, v121
	v_add_f32_e32 v121, v122, v123
	v_add_f32_e32 v231, v120, v121
	v_mov_b32_e32 v232, v231
	v_cvt_pk_bf16_f32 v96, v96, v97
	v_cvt_pk_bf16_f32 v97, v98, v99
	s_waitcnt lgkmcnt(8)
	v_mfma_f32_32x32x16_bf16 v[144:159], v[244:247], v[174:177], v[144:159]
	v_cvt_pk_bf16_f32 v98, v100, v101
	v_cvt_pk_bf16_f32 v99, v102, v103
	v_cvt_pk_bf16_f32 v120, v104, v105
	v_cvt_pk_bf16_f32 v121, v106, v107
	v_cvt_pk_bf16_f32 v122, v108, v109
	v_cvt_pk_bf16_f32 v123, v110, v111
	v_permlane32_swap_b32_e32 v96, v98
	v_permlane32_swap_b32_e32 v97, v99
	v_cvt_pk_bf16_f32 v104, v112, v113
	v_cvt_pk_bf16_f32 v105, v114, v115
	v_cvt_pk_bf16_f32 v106, v116, v117
	v_cvt_pk_bf16_f32 v107, v118, v119
	s_waitcnt lgkmcnt(0)
	v_mfma_f32_32x32x16_bf16 v[0:15], v[96:99], v[64:67], v[0:15]
	v_permlane32_swap_b32_e32 v120, v122
	v_permlane32_swap_b32_e32 v121, v123
	v_cvt_pk_bf16_f32 v100, v190, v191
	v_cvt_pk_bf16_f32 v101, v192, v193
	v_cvt_pk_bf16_f32 v102, v124, v125
	v_cvt_pk_bf16_f32 v103, v126, v127
	v_mfma_f32_32x32x16_bf16 v[0:15], v[120:123], v[68:71], v[0:15]
	v_permlane32_swap_b32_e32 v104, v106
	v_permlane32_swap_b32_e32 v105, v107
	ds_read_b64_tr_b16 v[236:237], v234 offset:0x200
	ds_read_b64_tr_b16 v[238:239], v234 offset:0xa00
	ds_read_b64_tr_b16 v[240:241], v234 offset:0x1200
	ds_read_b64_tr_b16 v[242:243], v234 offset:0x1a00
	ds_read_b64_tr_b16 v[244:245], v234 offset:0x2200
	ds_read_b64_tr_b16 v[246:247], v234 offset:0x2a00
	ds_read_b64_tr_b16 v[190:191], v234 offset:0x3200
	ds_read_b64_tr_b16 v[192:193], v234 offset:0x3a00
	v_mfma_f32_32x32x16_bf16 v[0:15], v[104:107], v[72:75], v[0:15]
	v_permlane32_swap_b32_e32 v100, v102
	v_permlane32_swap_b32_e32 v101, v103
	v_permlane32_swap_b32_e32 v231, v232
	v_max_f32_e32 v108, v128, v129
	v_max3_f32 v109, v130, v131, v145
	v_max3_f32 v108, v108, v144, v146
	v_max3_f32 v108, v108, v147, v132
	v_max3_f32 v109, v109, v134, v135
	v_mfma_f32_32x32x16_bf16 v[0:15], v[100:103], v[76:79], v[0:15]
	v_max3_f32 v208, v108, v133, v148
	v_max3_f32 v209, v109, v150, v151
	ds_read_b64_tr_b16 v[124:125], v234 offset:0x400
	ds_read_b64_tr_b16 v[126:127], v234 offset:0xc00
	ds_read_b64_tr_b16 v[116:117], v234 offset:0x1400
	ds_read_b64_tr_b16 v[118:119], v234 offset:0x1c00
	ds_read_b64_tr_b16 v[112:113], v234 offset:0x2400
	ds_read_b64_tr_b16 v[114:115], v234 offset:0x2c00
	ds_read_b64_tr_b16 v[108:109], v234 offset:0x3400
	ds_read_b64_tr_b16 v[110:111], v234 offset:0x3c00
	s_waitcnt lgkmcnt(8)
	v_mfma_f32_32x32x16_bf16 v[48:63], v[96:99], v[236:239], v[48:63]
	v_max3_f32 v208, v208, v149, v136
	v_max3_f32 v209, v209, v138, v139
	v_max3_f32 v208, v208, v137, v152
	v_max3_f32 v209, v209, v154, v155
	v_max3_f32 v208, v208, v153, v140
	v_max3_f32 v209, v209, v142, v143
	v_max3_f32 v208, v208, v141, v156
	v_mfma_f32_32x32x16_bf16 v[48:63], v[120:123], v[240:243], v[48:63]
	v_max3_f32 v209, v209, v158, v159
	v_max3_f32 v208, v208, v157, v209
	v_mov_b32_e32 v209, v208
	s_nop 1
	v_permlane32_swap_b32_e32 v208, v209
	v_mfma_f32_32x32x16_bf16 v[48:63], v[104:107], v[244:247], v[48:63]
	v_max_f32_e32 v233, v208, v209
	s_mov_b32 s2, 0x4138aa3b
	v_cmp_ge_f32_e32 vcc, s2, v233
	v_mfma_f32_32x32x16_bf16 v[48:63], v[100:103], v[190:193], v[48:63]
	s_cmp_eq_u64 vcc, exec
	s_cbranch_scc0 .LBB0_836
	v_mov_b32_e32 v233, 1.0

; #define SBAR() __builtin_amdgcn_sched_barrier(0)
; #define SLOAD(k0) do { vs0 = *reinterpret_cast<const bf16x8*>(&Vh[(size_t)((k0) + sr) * DM + sc]); vs1 = *reinterpret_cast<const bf16x8*>(&Vh[(size_t)((k0) + 32 + sr) * DM + sc]); \
;     ks = *reinterpret_cast<const bf16x8*>(&Kh[(size_t)((k0) + kr) * DM + kc]); } while (0)
; __device__ __forceinline__ void diff_pass(const bf16_t* __restrict__ Qb, const bf16_t* __restrict__ Kh, const bf16_t* __restrict__ Vh, int seq, char* lds, f32x16 (&o)[4], const int wave_) {
;     ...
;         SLOAD((j + 2) * 64);
;         SBAR(); qkt64c(pA0, pA1, K_lds + s_cur * SHM_K64, qr, negm, r32, hi); FIN(pB0, pB1, alB); SBAR();
;         YSEG(pA0, pA1, alA, s_prev);
.LBB0_829:
	s_waitcnt lgkmcnt(0)
	v_add_u32_e32 v102, s2, v223
	v_add_u32_e32 v103, s2, v226
	v_add_u32_e32 v104, s2, v228
	v_add_u32_e32 v105, s2, v229
	s_barrier
	ds_read_b128 v[112:115], v102 offset:49152
	ds_read_b128 v[116:119], v103 offset:49152
	ds_read_b128 v[120:123], v104 offset:49152
	ds_read_b128 v[124:127], v105 offset:49152
	ds_read_b128 v[190:193], v102 offset:53248
	ds_read_b128 v[202:205], v103 offset:53248
	ds_read_b128 v[234:237], v104 offset:53248
	ds_read_b128 v[238:241], v105 offset:53248
	global_load_dwordx4 v[178:181], v195, s[16:17]
	global_load_dwordx4 v[182:185], v255, s[16:17]
	global_load_dwordx4 v[186:189], v194, s[14:15]
	s_add_u32 s16, s16, 0x20000
	s_addc_u32 s17, s17, 0
	s_add_u32 s14, s14, 0x20000
	s_addc_u32 s15, s15, 0
	v_exp_f32_e32 v208, v152
	v_exp_f32_e32 v209, v153
	v_add_f32_e32 v152, v128, v129
	v_add_f32_e32 v153, v130, v131
	s_waitcnt lgkmcnt(7)
	v_mfma_f32_32x32x16_bf16 v[96:111], v[112:115], v[162:165], v[80:95]
	v_exp_f32_e32 v210, v154
	v_add_f32_e32 v152, v152, v153
	v_add_f32_e32 v153, v132, v133
	v_add_f32_e32 v154, v134, v135
	v_exp_f32_e32 v211, v155
	s_waitcnt lgkmcnt(6)
	v_mfma_f32_32x32x16_bf16 v[96:111], v[116:119], v[166:169], v[96:111]
	v_add_f32_e32 v153, v153, v154
	v_add_f32_e32 v154, v136, v137
	v_add_f32_e32 v155, v138, v139
	v_add_f32_e32 v154, v154, v155
	v_add_f32_e32 v155, v140, v141
	s_waitcnt lgkmcnt(5)
	v_mfma_f32_32x32x16_bf16 v[96:111], v[120:123], v[170:173], v[96:111]
	v_exp_f32_e32 v156, v156
	v_exp_f32_e32 v157, v157
	v_exp_f32_e32 v158, v158
	v_exp_f32_e32 v159, v159
	s_waitcnt lgkmcnt(4)
	v_mfma_f32_32x32x16_bf16 v[96:111], v[124:127], v[174:177], v[96:111]
	s_waitcnt lgkmcnt(3)
	v_mfma_f32_32x32x16_bf16 v[112:127], v[190:193], v[162:165], v[80:95]
	v_add_f32_e32 v190, v142, v143
	v_add_f32_e32 v155, v155, v190
	v_add_f32_e32 v190, v144, v145
	v_add_f32_e32 v191, v146, v147
	v_add_f32_e32 v190, v190, v191
	v_add_f32_e32 v152, v152, v190
	v_add_f32_e32 v190, v148, v149
	s_waitcnt lgkmcnt(2)
	v_mfma_f32_32x32x16_bf16 v[112:127], v[202:205], v[166:169], v[112:127]
	v_lshl_add_u32 v205, s42, 14, v217
	ds_read_b64_tr_b16 v[64:65], v205 offset:0
	ds_read_b64_tr_b16 v[66:67], v205 offset:0x800
	ds_read_b64_tr_b16 v[68:69], v205 offset:0x1000
	ds_read_b64_tr_b16 v[70:71], v205 offset:0x1800
	ds_read_b64_tr_b16 v[72:73], v205 offset:0x2000
	ds_read_b64_tr_b16 v[74:75], v205 offset:0x2800
	ds_read_b64_tr_b16 v[76:77], v205 offset:0x3000
	ds_read_b64_tr_b16 v[78:79], v205 offset:0x3800
	v_add_f32_e32 v191, v150, v151
	v_add_f32_e32 v190, v190, v191
	v_add_f32_e32 v153, v153, v190
	v_add_f32_e32 v190, v208, v209
	v_add_f32_e32 v191, v210, v211
	v_add_f32_e32 v190, v190, v191
	v_add_f32_e32 v154, v154, v190
	s_waitcnt lgkmcnt(9)
	v_mfma_f32_32x32x16_bf16 v[112:127], v[234:237], v[170:173], v[112:127]
	v_add_f32_e32 v190, v156, v157
	v_add_f32_e32 v191, v158, v159
	v_add_f32_e32 v190, v190, v191
	v_add_f32_e32 v155, v155, v190
	v_add_f32_e32 v152, v152, v153
	v_add_f32_e32 v153, v154, v155
	v_add_f32_e32 v203, v152, v153
	s_waitcnt lgkmcnt(8)
	v_mfma_f32_32x32x16_bf16 v[112:127], v[238:241], v[174:177], v[112:127]
	v_mov_b32_e32 v204, v203
	v_cvt_pk_bf16_f32 v152, v128, v129
	v_cvt_pk_bf16_f32 v153, v130, v131
	v_cvt_pk_bf16_f32 v154, v132, v133
	v_cvt_pk_bf16_f32 v155, v134, v135
	v_cvt_pk_bf16_f32 v136, v136, v137
	v_cvt_pk_bf16_f32 v137, v138, v139
	v_cvt_pk_bf16_f32 v138, v140, v141
	v_cvt_pk_bf16_f32 v139, v142, v143
	v_permlane32_swap_b32_e32 v152, v154
	v_permlane32_swap_b32_e32 v153, v155
	v_cvt_pk_bf16_f32 v132, v144, v145
	v_cvt_pk_bf16_f32 v133, v146, v147
	v_cvt_pk_bf16_f32 v134, v148, v149
	v_cvt_pk_bf16_f32 v135, v150, v151
	s_waitcnt lgkmcnt(0)
	v_mfma_f32_32x32x16_bf16 v[0:15], v[152:155], v[64:67], v[0:15]
	v_permlane32_swap_b32_e32 v136, v138
	v_permlane32_swap_b32_e32 v137, v139
	v_cvt_pk_bf16_f32 v128, v208, v209
	v_cvt_pk_bf16_f32 v129, v210, v211
	v_cvt_pk_bf16_f32 v130, v156, v157
	v_cvt_pk_bf16_f32 v131, v158, v159
	v_mfma_f32_32x32x16_bf16 v[0:15], v[136:139], v[68:71], v[0:15]
	v_permlane32_swap_b32_e32 v132, v134
	v_permlane32_swap_b32_e32 v133, v135
	ds_read_b64_tr_b16 v[190:191], v205 offset:0x200
	ds_read_b64_tr_b16 v[192:193], v205 offset:0xa00
	ds_read_b64_tr_b16 v[234:235], v205 offset:0x1200
	ds_read_b64_tr_b16 v[236:237], v205 offset:0x1a00
	ds_read_b64_tr_b16 v[238:239], v205 offset:0x2200
	ds_read_b64_tr_b16 v[240:241], v205 offset:0x2a00
	ds_read_b64_tr_b16 v[242:243], v205 offset:0x3200
	ds_read_b64_tr_b16 v[244:245], v205 offset:0x3a00
	v_mfma_f32_32x32x16_bf16 v[0:15], v[132:135], v[72:75], v[0:15]
	v_permlane32_swap_b32_e32 v128, v130
	v_permlane32_swap_b32_e32 v129, v131
	v_permlane32_swap_b32_e32 v203, v204
	v_max_f32_e32 v140, v96, v97
	v_max3_f32 v140, v140, v112, v114
	v_max3_f32 v141, v98, v99, v113
	v_max3_f32 v140, v140, v115, v100
	v_max3_f32 v141, v141, v102, v103
	v_mfma_f32_32x32x16_bf16 v[0:15], v[128:131], v[76:79], v[0:15]
	v_max3_f32 v202, v140, v101, v116
	v_max3_f32 v208, v141, v118, v119
	ds_read_b64_tr_b16 v[156:157], v205 offset:0x400
	ds_read_b64_tr_b16 v[158:159], v205 offset:0xc00
	ds_read_b64_tr_b16 v[148:149], v205 offset:0x1400
	ds_read_b64_tr_b16 v[150:151], v205 offset:0x1c00
	ds_read_b64_tr_b16 v[144:145], v205 offset:0x2400
	ds_read_b64_tr_b16 v[146:147], v205 offset:0x2c00
	ds_read_b64_tr_b16 v[140:141], v205 offset:0x3400
	ds_read_b64_tr_b16 v[142:143], v205 offset:0x3c00
	s_waitcnt lgkmcnt(8)
	v_mfma_f32_32x32x16_bf16 v[48:63], v[152:155], v[190:193], v[48:63]
	v_max3_f32 v190, v202, v117, v104
	v_max3_f32 v191, v208, v106, v107
	v_max3_f32 v190, v190, v105, v120
	v_max3_f32 v191, v191, v122, v123
	v_max3_f32 v190, v190, v121, v108
	v_max3_f32 v191, v191, v110, v111
	v_max3_f32 v190, v190, v109, v124
	v_mfma_f32_32x32x16_bf16 v[48:63], v[136:139], v[234:237], v[48:63]
	v_max3_f32 v191, v191, v126, v127
	v_max3_f32 v190, v190, v125, v191
	v_mov_b32_e32 v191, v190
	s_nop 1
	v_permlane32_swap_b32_e32 v190, v191
	v_mfma_f32_32x32x16_bf16 v[48:63], v[132:135], v[238:241], v[48:63]
	v_max_f32_e32 v234, v190, v191
	s_mov_b32 s2, 0x4138aa3b
	v_cmp_ge_f32_e32 vcc, s2, v234
	v_mfma_f32_32x32x16_bf16 v[48:63], v[128:131], v[242:245], v[48:63]
	s_cmp_eq_u64 vcc, exec
	v_mov_b32_e32 v202, 1.0
	s_cbranch_scc0 .LBB0_837

; #define SBAR() __builtin_amdgcn_sched_barrier(0)
; #define SLOAD(k0) do { vs0 = *reinterpret_cast<const bf16x8*>(&Vh[(size_t)((k0) + sr) * DM + sc]); vs1 = *reinterpret_cast<const bf16x8*>(&Vh[(size_t)((k0) + 32 + sr) * DM + sc]); \
;     ks = *reinterpret_cast<const bf16x8*>(&Kh[(size_t)((k0) + kr) * DM + kc]); } while (0)
; #define SWRITE(s) do { *(bf16x8*)(V_lds + (s) * SHM_V + vst0) = vs0; *(bf16x8*)(V_lds + (s) * SHM_V + vst1) = vs1; *(bf16x8*)(K_lds + (s) * SHM_K64 + kst) = ks; } while (0)
; #define RESC(a) do { if (__any((a) < 1.f)) { if (hi == 0) al_l[r32] = (a); asm volatile("s_waitcnt lgkmcnt(0)" ::: "memory"); \
;     _Pragma("unroll") for (int d = 0; d < 4; ++d) _Pragma("unroll") for (int r = 0; r < 16; ++r) o[d][r] *= al_l[crow(r, hi)]; } } while (0)
; #define ROT() do { s_prev = s_cur; s_cur = s_next; s_next = (s_next == DA_NBUF - 1) ? 0 : s_next + 1; } while (0)
; __device__ __forceinline__ void diff_pass(const bf16_t* __restrict__ Qb, const bf16_t* __restrict__ Kh, const bf16_t* __restrict__ Vh, int seq, char* lds, f32x16 (&o)[4], const int wave_) {
;     ...
;         SWRITE(s_next); RESC(alB); __syncthreads(); ROT();
;         SLOAD((j + 2) * 64);
;         SBAR(); qkt64c(pA0, pA1, K_lds + s_cur * SHM_K64, qr, negm, r32, hi); FIN(pB0, pB1, alB); SBAR();
;         YSEG(pA0, pA1, alA, s_prev);
;         SWRITE(s_next); RESC(alA); __syncthreads(); ROT();
;     }
.LBB0_834:
	s_add_i32 s2, s42, 1
	v_add_f32_e32 v128, v231, v232
	s_cmp_lg_u32 s42, 2
	v_fmac_f32_e32 v128, v215, v230
	v_add_f32_e32 v215, v203, v204
	s_cselect_b32 s2, s2, 0
	s_add_i32 s40, s40, 2
	v_fmac_f32_e32 v215, v128, v233
	s_lshl_b32 s3, s42, 13
	s_cmp_gt_u32 s40, 28
	v_add_u32_e32 v128, s3, v223
	v_add_u32_e32 v129, s3, v226
	v_add_u32_e32 v130, s3, v228
	v_add_u32_e32 v131, s3, v229
	v_mov_b32_e32 v230, v202
	s_mov_b32 s12, s41
	s_mov_b32 s41, s2
	s_waitcnt lgkmcnt(0)
	s_barrier
	s_cbranch_scc1 .LBB0_838
	s_branch .Latt9_p1_top

; #define SBAR() __builtin_amdgcn_sched_barrier(0)
; __device__ __forceinline__ int crow(int r, int hi) { return (r & 3) + 8 * (r >> 2) + 4 * hi; }
; __device__ __forceinline__ void diff_pass(const bf16_t* __restrict__ Qb, const bf16_t* __restrict__ Kh, const bf16_t* __restrict__ Vh, int seq, char* lds, f32x16 (&o)[4], const int wave_) {
;     ...
;     FIN(pB0, pB1, alB); SBAR();
;     pv_d0(o, vb0 + s_cur * SHM_V, pa0, pa1, pa2, pa3);
;     if (hi == 0) li_l[r32] = l_reg; asm volatile("s_waitcnt lgkmcnt(0)" ::: "memory");
; #pragma unroll
;     for (int r = 0; r < 16; ++r) { const float rl = __builtin_amdgcn_rcpf(li_l[crow(r, hi)]);
; #pragma unroll
;         for (int d = 0; d < 4; ++d) o[d][r] *= rl; }
.LBB0_843:
	v_exp_f32_e32 v96, v72
	v_exp_f32_e32 v97, v73
	v_add_f32_e32 v72, v80, v81
	v_add_f32_e32 v73, v82, v83
	v_exp_f32_e32 v98, v74
	v_add_f32_e32 v72, v72, v73
	v_add_f32_e32 v73, v84, v85
	v_add_f32_e32 v74, v86, v87
	v_exp_f32_e32 v99, v75
	v_add_f32_e32 v73, v73, v74
	v_add_f32_e32 v74, v88, v89
	v_add_f32_e32 v75, v90, v91
	v_exp_f32_e32 v100, v76
	v_add_f32_e32 v74, v74, v75
	v_add_f32_e32 v75, v92, v93
	v_add_f32_e32 v76, v94, v95
	v_exp_f32_e32 v101, v77
	v_add_f32_e32 v75, v75, v76
	v_add_f32_e32 v76, v64, v65
	v_add_f32_e32 v77, v66, v67
	v_add_f32_e32 v76, v76, v77
	v_exp_f32_e32 v102, v78
	v_exp_f32_e32 v103, v79
	v_add_f32_e32 v72, v72, v76
	v_add_f32_e32 v76, v68, v69
	v_add_f32_e32 v77, v70, v71
	v_add_f32_e32 v76, v76, v77
	v_add_f32_e32 v73, v73, v76
	v_add_f32_e32 v76, v96, v97
	v_add_f32_e32 v77, v98, v99
	v_add_f32_e32 v76, v76, v77
	v_add_f32_e32 v74, v74, v76
	v_add_f32_e32 v76, v100, v101
	v_add_f32_e32 v77, v102, v103
	v_add_f32_e32 v76, v76, v77
	v_add_f32_e32 v75, v75, v76
	v_add_f32_e32 v72, v72, v73
	v_add_f32_e32 v73, v74, v75
	v_add_f32_e32 v72, v72, v73
	v_mov_b32_e32 v73, v72
	s_nop 1
	v_permlane32_swap_b32_e32 v72, v73
	v_cvt_pk_bf16_f32 v74, v80, v81
	v_cvt_pk_bf16_f32 v75, v82, v83
	v_cvt_pk_bf16_f32 v76, v84, v85
	v_cvt_pk_bf16_f32 v77, v86, v87
	v_cvt_pk_bf16_f32 v78, v88, v89
	v_cvt_pk_bf16_f32 v79, v90, v91
	v_cvt_pk_bf16_f32 v80, v92, v93
	v_cvt_pk_bf16_f32 v81, v94, v95
	v_cvt_pk_bf16_f32 v64, v64, v65
	v_cvt_pk_bf16_f32 v65, v66, v67
	v_cvt_pk_bf16_f32 v66, v68, v69
	v_cvt_pk_bf16_f32 v67, v70, v71
	v_cvt_pk_bf16_f32 v68, v96, v97
	v_cvt_pk_bf16_f32 v69, v98, v99
	v_cvt_pk_bf16_f32 v70, v100, v101
	v_cvt_pk_bf16_f32 v71, v102, v103
	s_nop 0
	v_permlane32_swap_b32_e32 v74, v76
	v_permlane32_swap_b32_e32 v75, v77
	v_permlane32_swap_b32_e32 v78, v80
	v_permlane32_swap_b32_e32 v79, v81
	v_permlane32_swap_b32_e32 v64, v66
	v_permlane32_swap_b32_e32 v65, v67
	v_permlane32_swap_b32_e32 v68, v70
	v_permlane32_swap_b32_e32 v69, v71
	s_cmp_lg_u32 0, -1
	s_cselect_b32 s2, 0, 0
	s_addk_i32 s2, 0x4000
	v_add_u32_e32 v98, s2, v216
	ds_read_b64_tr_b16 v[82:83], v98 offset:0
	ds_read_b64_tr_b16 v[84:85], v98 offset:0x800
	ds_read_b64_tr_b16 v[86:87], v98 offset:0x1000
	ds_read_b64_tr_b16 v[88:89], v98 offset:0x1800
	ds_read_b64_tr_b16 v[90:91], v98 offset:0x2000
	ds_read_b64_tr_b16 v[92:93], v98 offset:0x2800
	ds_read_b64_tr_b16 v[94:95], v98 offset:0x3000
	ds_read_b64_tr_b16 v[96:97], v98 offset:0x3800
	s_waitcnt lgkmcnt(0)
	s_nop 0
	v_mfma_f32_32x32x16_bf16 v[0:15], v[74:77], v[82:85], v[0:15]
	ds_read_b64_tr_b16 v[82:83], v98 offset:0x200
	ds_read_b64_tr_b16 v[84:85], v98 offset:0xa00
	v_mfma_f32_32x32x16_bf16 v[0:15], v[78:81], v[86:89], v[0:15]
	ds_read_b64_tr_b16 v[86:87], v98 offset:0x1200
	ds_read_b64_tr_b16 v[88:89], v98 offset:0x1a00
	v_mfma_f32_32x32x16_bf16 v[0:15], v[64:67], v[90:93], v[0:15]
	ds_read_b64_tr_b16 v[90:91], v98 offset:0x2200
	ds_read_b64_tr_b16 v[92:93], v98 offset:0x2a00
	v_mfma_f32_32x32x16_bf16 v[0:15], v[68:71], v[94:97], v[0:15]
	ds_read_b64_tr_b16 v[94:95], v98 offset:0x3200
	ds_read_b64_tr_b16 v[96:97], v98 offset:0x3a00
	s_waitcnt lgkmcnt(0)
	v_mfma_f32_32x32x16_bf16 v[48:63], v[74:77], v[82:85], v[48:63]
	ds_read_b64_tr_b16 v[82:83], v98 offset:0x400
	ds_read_b64_tr_b16 v[84:85], v98 offset:0xc00
	v_mfma_f32_32x32x16_bf16 v[48:63], v[78:81], v[86:89], v[48:63]
	ds_read_b64_tr_b16 v[86:87], v98 offset:0x1400
	ds_read_b64_tr_b16 v[88:89], v98 offset:0x1c00
	v_mfma_f32_32x32x16_bf16 v[48:63], v[64:67], v[90:93], v[48:63]
	ds_read_b64_tr_b16 v[90:91], v98 offset:0x2400
	ds_read_b64_tr_b16 v[92:93], v98 offset:0x2c00
	v_mfma_f32_32x32x16_bf16 v[48:63], v[68:71], v[94:97], v[48:63]
	ds_read_b64_tr_b16 v[94:95], v98 offset:0x3400
	ds_read_b64_tr_b16 v[96:97], v98 offset:0x3c00
	s_waitcnt lgkmcnt(0)
	v_mfma_f32_32x32x16_bf16 v[32:47], v[74:77], v[82:85], v[32:47]
	ds_read_b64_tr_b16 v[82:83], v98 offset:0x600
	ds_read_b64_tr_b16 v[84:85], v98 offset:0xe00
	v_mfma_f32_32x32x16_bf16 v[32:47], v[78:81], v[86:89], v[32:47]
	ds_read_b64_tr_b16 v[86:87], v98 offset:0x1600
	ds_read_b64_tr_b16 v[88:89], v98 offset:0x1e00
	v_mfma_f32_32x32x16_bf16 v[32:47], v[64:67], v[90:93], v[32:47]
	ds_read_b64_tr_b16 v[90:91], v98 offset:0x2600
	ds_read_b64_tr_b16 v[92:93], v98 offset:0x2e00
	v_mfma_f32_32x32x16_bf16 v[32:47], v[68:71], v[94:97], v[32:47]
	ds_read_b64_tr_b16 v[94:95], v98 offset:0x3600
	ds_read_b64_tr_b16 v[96:97], v98 offset:0x3e00
	s_waitcnt lgkmcnt(0)
	v_mfma_f32_32x32x16_bf16 v[16:31], v[74:77], v[82:85], v[16:31]
	v_mfma_f32_32x32x16_bf16 v[16:31], v[78:81], v[86:89], v[16:31]
	v_mfma_f32_32x32x16_bf16 v[16:31], v[64:67], v[90:93], v[16:31]
	v_mfma_f32_32x32x16_bf16 v[16:31], v[68:71], v[94:97], v[16:31]
	s_and_saveexec_b64 s[12:13], s[0:1]
	v_add_f32_e32 v64, v128, v129
	v_fmac_f32_e32 v64, v215, v202
	v_add_f32_e32 v65, v72, v73
	v_fmac_f32_e32 v65, v64, v130
	ds_write_b32 v214, v65
	s_or_b64 exec, exec, s[12:13]
	s_waitcnt lgkmcnt(0)
	v_add_u32_e32 v72, v213, v160
	ds_read_b128 v[64:67], v72
	ds_read_b128 v[68:71], v72 offset:32
	v_ashrrev_i32_e32 v214, 6, v207
	s_add_i32 s0, 0, 0x12800
	v_and_b32_e32 v213, 63, v207
	s_waitcnt lgkmcnt(1)
	v_rcp_f32_e32 v64, v64
	v_rcp_f32_e32 v65, v65
	v_lshl_add_u32 v215, v214, 13, s0
	v_lshl_add_u32 v216, v213, 2, v215
	v_mul_f32_e32 v73, v0, v64
	v_rcp_f32_e32 v0, v66
	v_mul_f32_e32 v48, v48, v64
	v_mul_f32_e32 v32, v32, v64
	v_mul_f32_e32 v16, v16, v64
	v_mul_f32_e32 v64, v1, v65
	v_mul_f32_e32 v49, v49, v65
	v_mul_f32_e32 v33, v33, v65
	v_mul_f32_e32 v17, v17, v65
	v_mul_f32_e32 v65, v2, v0
	v_rcp_f32_e32 v1, v67
	v_mul_f32_e32 v50, v50, v0
	v_mul_f32_e32 v34, v34, v0
	v_mul_f32_e32 v18, v18, v0
	s_waitcnt lgkmcnt(0)
; __device__ __forceinline__ unsigned cvt_pk_bf16(float lo, float hi) { unsigned r; asm volatile("v_cvt_pk_bf16_f32 %0, %1, %2" : "=v"(r) : "v"(lo), "v"(hi)); return r; }
; __device__ __forceinline__ int crow(int r, int hi) { return (r & 3) + 8 * (r >> 2) + 4 * hi; }
; __device__ __forceinline__ void diff_pass(const bf16_t* __restrict__ Qb, const bf16_t* __restrict__ Kh, const bf16_t* __restrict__ Vh, int seq, char* lds, f32x16 (&o)[4], const int wave_) {
;     ...
;     for (int r = 0; r < 16; ++r) { const float rl = __builtin_amdgcn_rcpf(li_l[crow(r, hi)]);
; #pragma unroll
;         for (int d = 0; d < 4; ++d) o[d][r] *= rl; }
; __device__ __forceinline__ void diff_unit(int b, int h, int qb, const bf16_t* Q, const bf16_t* K, const bf16_t* V, bf16_t* YA, float lam, float omli, const float* subln, char* lds, const int wave_) {
;     ...
;     unsigned* park = (unsigned*)(lds + DA_LDS) + wid * 2048 + lane;
; #pragma unroll
;     for (int d = 0; d < 4; ++d)
; #pragma unroll
;         for (int r = 0; r < 8; ++r) park[(d * 8 + r) * 64] = cvt_pk_bf16(o[d][2 * r], o[d][2 * r + 1]);
	v_rcp_f32_e32 v0, v68
	v_mul_f32_e32 v66, v3, v1
	v_mul_f32_e32 v51, v51, v1
	v_mul_f32_e32 v35, v35, v1
	v_mul_f32_e32 v19, v19, v1
	v_mul_f32_e32 v67, v4, v0
	v_rcp_f32_e32 v1, v69
	v_rcp_f32_e32 v4, v70
	v_rcp_f32_e32 v70, v71
	v_mul_f32_e32 v52, v52, v0
	v_mul_f32_e32 v36, v36, v0
	v_mul_f32_e32 v20, v20, v0
	v_mul_f32_e32 v68, v5, v1
	v_mul_f32_e32 v53, v53, v1
	v_mul_f32_e32 v37, v37, v1
	v_mul_f32_e32 v21, v21, v1
	v_mul_f32_e32 v69, v6, v4
	v_mul_f32_e32 v54, v54, v4
	ds_read_b128 v[0:3], v72 offset:64
	v_mul_f32_e32 v38, v38, v4
	v_mul_f32_e32 v22, v22, v4
	v_mul_f32_e32 v71, v7, v70
	ds_read_b128 v[4:7], v72 offset:96
	s_waitcnt lgkmcnt(1)
	v_rcp_f32_e32 v0, v0
	v_rcp_f32_e32 v1, v1
	v_rcp_f32_e32 v2, v2
	v_rcp_f32_e32 v3, v3
	s_waitcnt lgkmcnt(0)
	v_rcp_f32_e32 v4, v4
	v_rcp_f32_e32 v5, v5
	v_rcp_f32_e32 v6, v6
	v_rcp_f32_e32 v7, v7
	v_mul_f32_e32 v8, v8, v0
	v_mul_f32_e32 v56, v56, v0
	v_mul_f32_e32 v40, v40, v0
	v_mul_f32_e32 v0, v24, v0
	v_mul_f32_e32 v9, v9, v1
	v_mul_f32_e32 v24, v57, v1
	v_mul_f32_e32 v41, v41, v1
	v_mul_f32_e32 v1, v25, v1
	v_mul_f32_e32 v10, v10, v2
	v_mul_f32_e32 v25, v58, v2
	v_mul_f32_e32 v42, v42, v2
	v_mul_f32_e32 v2, v26, v2
	v_mul_f32_e32 v11, v11, v3
	v_mul_f32_e32 v26, v59, v3
	v_mul_f32_e32 v43, v43, v3
	v_mul_f32_e32 v3, v27, v3
	v_mul_f32_e32 v12, v12, v4
	v_mul_f32_e32 v27, v60, v4
	v_mul_f32_e32 v44, v44, v4
	v_mul_f32_e32 v4, v28, v4
	v_mul_f32_e32 v13, v13, v5
	v_mul_f32_e32 v28, v61, v5
	v_mul_f32_e32 v45, v45, v5
	v_mul_f32_e32 v5, v29, v5
	v_mul_f32_e32 v14, v14, v6
	v_mul_f32_e32 v29, v62, v6
	v_mul_f32_e32 v46, v46, v6
	v_mul_f32_e32 v6, v30, v6
	v_mul_f32_e32 v15, v15, v7
	v_mul_f32_e32 v30, v63, v7
	v_mul_f32_e32 v47, v47, v7
	v_mul_f32_e32 v7, v31, v7
	v_cvt_pk_bf16_f32 v31, v73, v64
	ds_write_b32 v216, v31
	v_cvt_pk_bf16_f32 v31, v65, v66
	ds_write_b32 v216, v31 offset:256
	v_cvt_pk_bf16_f32 v31, v67, v68
	ds_write_b32 v216, v31 offset:512
	v_cvt_pk_bf16_f32 v31, v69, v71
	ds_write_b32 v216, v31 offset:768
	v_cvt_pk_bf16_f32 v8, v8, v9
	ds_write_b32 v216, v8 offset:1024
	v_cvt_pk_bf16_f32 v8, v10, v11
	ds_write_b32 v216, v8 offset:1280
	v_cvt_pk_bf16_f32 v8, v12, v13
	ds_write_b32 v216, v8 offset:1536
	v_cvt_pk_bf16_f32 v8, v14, v15
	ds_write_b32 v216, v8 offset:1792
	v_cvt_pk_bf16_f32 v8, v48, v49
	ds_write_b32 v216, v8 offset:2048
	v_cvt_pk_bf16_f32 v8, v50, v51
	ds_write_b32 v216, v8 offset:2304
	v_cvt_pk_bf16_f32 v8, v52, v53
	v_mul_f32_e32 v55, v55, v70
	ds_write_b32 v216, v8 offset:2560
	v_cvt_pk_bf16_f32 v8, v54, v55
	ds_write_b32 v216, v8 offset:2816
	v_cvt_pk_bf16_f32 v8, v56, v24
	ds_write_b32 v216, v8 offset:3072
	v_cvt_pk_bf16_f32 v8, v25, v26
	ds_write_b32 v216, v8 offset:3328
	v_cvt_pk_bf16_f32 v8, v27, v28
	ds_write_b32 v216, v8 offset:3584
	v_cvt_pk_bf16_f32 v8, v29, v30
	ds_write_b32 v216, v8 offset:3840
	v_cvt_pk_bf16_f32 v8, v32, v33
	ds_write_b32 v216, v8 offset:4096
	v_cvt_pk_bf16_f32 v8, v34, v35
	ds_write_b32 v216, v8 offset:4352
	v_cvt_pk_bf16_f32 v8, v36, v37
	v_mul_f32_e32 v39, v39, v70
	ds_write_b32 v216, v8 offset:4608
	v_cvt_pk_bf16_f32 v8, v38, v39
	ds_write_b32 v216, v8 offset:4864
	v_cvt_pk_bf16_f32 v8, v40, v41
	ds_write_b32 v216, v8 offset:5120
	v_cvt_pk_bf16_f32 v8, v42, v43
	ds_write_b32 v216, v8 offset:5376
	v_cvt_pk_bf16_f32 v8, v44, v45
	ds_write_b32 v216, v8 offset:5632
	v_cvt_pk_bf16_f32 v8, v46, v47
	ds_write_b32 v216, v8 offset:5888
	v_cvt_pk_bf16_f32 v8, v16, v17
	ds_write_b32 v216, v8 offset:6144
	v_cvt_pk_bf16_f32 v8, v18, v19
	ds_write_b32 v216, v8 offset:6400
	v_cvt_pk_bf16_f32 v8, v20, v21
	v_mul_f32_e32 v23, v23, v70
	ds_write_b32 v216, v8 offset:6656
	v_cvt_pk_bf16_f32 v8, v22, v23
	ds_write_b32 v216, v8 offset:6912
	v_cvt_pk_bf16_f32 v0, v0, v1
	ds_write_b32 v216, v0 offset:7168
	v_cvt_pk_bf16_f32 v0, v2, v3
	ds_write_b32 v216, v0 offset:7424
	v_cvt_pk_bf16_f32 v0, v4, v5
	ds_write_b32 v216, v0 offset:7680
	v_cvt_pk_bf16_f32 v0, v6, v7
	s_mov_b32 s0, -1
	ds_write_b32 v216, v0 offset:7936
	v_mov_b32_e32 v5, v161
	v_mbcnt_lo_u32_b32 v0, s0, 0
	v_mbcnt_hi_u32_b32 v0, s0, v0
	v_or_b32_e32 v68, s55, v0
	s_movk_i32 s0, 0xffe0
	v_ashrrev_i32_e32 v0, 1, v68
	v_bfi_b32 v0, s0, v0, v68
	v_ashrrev_i32_e32 v1, 31, v0
	v_lshlrev_b64 v[0:1], 11, v[0:1]
	v_lshrrev_b32_e32 v2, 1, v68
	v_ashrrev_i32_e32 v12, 4, v68
	v_lshl_add_u64 v[0:1], s[34:35], 0, v[0:1]
	v_and_b32_e32 v160, 16, v2
	v_lshlrev_b32_e32 v24, 3, v68
	v_ashrrev_i32_e32 v13, 31, v12
	v_lshl_add_u64 v[0:1], v[0:1], 0, v[160:161]
	v_and_b32_e32 v2, 0x78, v24
	v_lshlrev_b64 v[48:49], 11, v[12:13]
	v_lshl_add_u64 v[0:1], s[30:31], 0, v[48:49]
	v_lshlrev_b32_e32 v4, 1, v2
	v_add_u32_e32 v14, 32, v12
	v_ashrrev_i32_e32 v16, 3, v68
	v_lshl_add_u64 v[18:19], v[0:1], 0, v[4:5]
	s_waitcnt lgkmcnt(0)
	s_barrier
; #define SLOAD(k0) do { vs0 = *reinterpret_cast<const bf16x8*>(&Vh[(size_t)((k0) + sr) * DM + sc]); vs1 = *reinterpret_cast<const bf16x8*>(&Vh[(size_t)((k0) + 32 + sr) * DM + sc]); \
;     ks = *reinterpret_cast<const bf16x8*>(&Kh[(size_t)((k0) + kr) * DM + kc]); } while (0)
; #define SWRITE(s) do { *(bf16x8*)(V_lds + (s) * SHM_V + vst0) = vs0; *(bf16x8*)(V_lds + (s) * SHM_V + vst1) = vs1; *(bf16x8*)(K_lds + (s) * SHM_K64 + kst) = ks; } while (0)
; #define EX2(x) x = __builtin_amdgcn_exp2f(x)
; __device__ __forceinline__ void diff_pass(const bf16_t* __restrict__ Qb, const bf16_t* __restrict__ Kh, const bf16_t* __restrict__ Vh, int seq, char* lds, f32x16 (&o)[4], const int wave_) {
;     ...
;     __syncthreads();
;     SLOAD(0); SWRITE(0); SLOAD(64); __syncthreads();
;     negm = f32x16{};
;     qkt64c(pA0, pA1, K_lds, qr, negm, r32, hi);
;     { const float pm = rowmax32(pA0, pA1); m_reg = pm; alA = 1.f;
; #pragma unroll
;       for (int r = 0; r < 16; ++r) { pA0[r] -= pm; pA1[r] -= pm; negm[r] = -pm; }
; #pragma unroll
;       for (int r = 0; r < 16; ++r) EX2(pA0[r]);
; #pragma unroll
;       for (int r = 0; r < 8; ++r) EX2(pA1[r]); }
;     SWRITE(1); __syncthreads();
	v_ashrrev_i32_e32 v15, 31, v14
	v_ashrrev_i32_e32 v17, 31, v16
	v_lshlrev_b32_e32 v64, 4, v68
	v_lshlrev_b64 v[6:7], 11, v[14:15]
	v_lshlrev_b64 v[50:51], 11, v[16:17]
	v_lshl_add_u64 v[6:7], s[30:31], 0, v[6:7]
	v_and_b32_e32 v20, 0x70, v64
	v_lshl_add_u64 v[8:9], s[28:29], 0, v[50:51]
	v_mov_b32_e32 v21, v161
	v_lshl_add_u64 v[4:5], v[6:7], 0, v[4:5]
	v_lshl_add_u64 v[22:23], v[8:9], 0, v[20:21]
	v_and_b32_e32 v13, 0xfffff0, v12
	v_lshlrev_b32_e32 v15, 1, v12
	v_and_or_b32 v13, v15, 8, v13
	v_lshrrev_b32_e32 v15, 1, v12
	v_lshrrev_b32_e32 v13, 1, v13
	v_bfe_u32 v17, v24, 5, 2
	v_and_b32_e32 v12, 3, v12
	v_or_b32_e32 v13, v13, v17
	v_and_or_b32 v12, v15, 4, v12
	v_lshlrev_b32_e32 v13, 9, v13
	v_lshlrev_b32_e32 v12, 6, v12
	v_and_b32_e32 v15, 48, v64
	v_or3_b32 v222, v13, v12, v15
	v_and_b32_e32 v13, 0xfffff0, v14
	v_lshlrev_b32_e32 v14, 1, v14
	v_and_or_b32 v13, v14, 8, v13
	v_lshrrev_b32_e32 v13, 1, v13
	v_or_b32_e32 v13, v13, v17
	v_add_u32_e32 v70, 0, v222
	s_mov_b32 s0, 0x20000
	v_lshlrev_b32_e32 v13, 9, v13
	v_or3_b32 v223, v13, v12, v15
	v_lshlrev_b32_e32 v12, 7, v16
	v_and_b32_e32 v13, 0x70, v68
	s_mov_b32 s1, 0x30000
	v_bitop3_b32 v224, v20, v12, v13 bitop3:0xde
	v_add_u32_e32 v71, 0, v223
	v_add_u32_e32 v225, 0, v224
	v_and_b32_e32 v69, 31, v68
	v_lshlrev_b32_e32 v12, 7, v69
	v_and_b32_e32 v13, 0x70, v24
	v_bitop3_b32 v227, v160, v12, v13 bitop3:0xde
	v_add_u32_e32 v226, 0, v227
	v_and_b32_e32 v72, 63, v68
	s_mov_b32 s12, 0
	s_mov_b32 s13, s12
	s_mov_b32 s14, s12
	s_mov_b32 s15, s12
	s_mov_b32 s16, s12
	s_mov_b32 s17, s12
	s_mov_b32 s18, s12
	s_mov_b32 s19, s12
	s_mov_b32 s20, s12
	s_mov_b32 s21, s12
	s_mov_b32 s22, s12
	s_mov_b32 s23, s12
	s_mov_b32 s24, s12
	s_mov_b32 s25, s12
	s_mov_b32 s26, s12
	s_mov_b32 s27, s12
	s_cmp_lg_u32 0, -1
	s_mov_b32 s29, 2
	s_mov_b32 s28, -1
	s_mov_b32 s30, 1
	v_mov_b32_e32 v234, 1.0
	v_mov_b32_e32 v219, 0
	s_waitcnt vmcnt(0)
	ds_write_b128 v70, v[178:181]
	v_add_co_u32_e32 v0, vcc, s0, v18
	s_nop 1
	v_addc_co_u32_e32 v1, vcc, 0, v19, vcc
	global_load_dwordx4 v[52:55], v[0:1], off
	v_add_co_u32_e32 v0, vcc, s1, v18
	s_waitcnt vmcnt(2)
	ds_write_b128 v71, v[182:185]
	v_addc_co_u32_e32 v1, vcc, 0, v19, vcc
	s_waitcnt vmcnt(1)
	ds_write_b128 v225, v[186:189] offset:49152
	v_add_co_u32_e32 v2, vcc, s0, v22
	v_and_b32_e32 v8, 0x3fffffc0, v68
	s_nop 0
	v_addc_co_u32_e32 v3, vcc, 0, v23, vcc
	global_load_dwordx4 v[56:59], v[0:1], off
	global_load_dwordx4 v[60:63], v[2:3], off offset:128
	s_waitcnt lgkmcnt(0)
	s_barrier
	ds_read_b128 v[0:3], v226 offset:49152
	ds_read_b128 v[4:7], v226 offset:53248
	s_waitcnt lgkmcnt(1)
	v_mfma_f32_32x32x16_bf16 v[32:47], v[0:3], v[162:165], 0
	v_or_b32_e32 v0, 32, v160
	v_bitop3_b32 v231, v0, v12, v13 bitop3:0xde
	v_add_u32_e32 v228, 0, v231
	v_lshl_add_u32 v217, v8, 2, s39
	s_cselect_b32 s0, 0, 0
	v_lshl_add_u32 v218, v69, 2, v217
	s_waitcnt lgkmcnt(0)
	v_mfma_f32_32x32x16_bf16 v[16:31], v[4:7], v[162:165], 0
	ds_read_b128 v[0:3], v228 offset:49152
	ds_read_b128 v[4:7], v228 offset:53248
	s_waitcnt lgkmcnt(1)
	v_mfma_f32_32x32x16_bf16 v[32:47], v[0:3], v[166:169], v[32:47]
	v_or_b32_e32 v0, 64, v160
	v_bitop3_b32 v232, v0, v12, v13 bitop3:0xde
	v_add_u32_e32 v229, 0, v232
	ds_read_b128 v[0:3], v229 offset:53248
	ds_read_b128 v[8:11], v229 offset:49152
	s_waitcnt lgkmcnt(2)
	v_mfma_f32_32x32x16_bf16 v[16:31], v[4:7], v[166:169], v[16:31]
	v_lshlrev_b32_e32 v4, 3, v72
	v_and_b32_e32 v5, 0xc0, v64
	v_lshlrev_b32_e32 v6, 1, v68
	v_and_or_b32 v5, v4, 24, v5
	v_and_b32_e32 v6, 32, v6
	v_and_b32_e32 v4, 0x100, v4
	v_or3_b32 v220, v5, v6, v4
	s_waitcnt lgkmcnt(0)
	v_mfma_f32_32x32x16_bf16 v[32:47], v[8:11], v[170:173], v[32:47]
	v_or_b32_e32 v4, 0x60, v160
	v_bitop3_b32 v233, v4, v12, v13 bitop3:0xde
	v_add_u32_e32 v230, 0, v233
	ds_read_b128 v[64:67], v230 offset:53248
	ds_read_b128 v[4:7], v230 offset:49152
	s_waitcnt vmcnt(2)
	ds_write_b128 v70, v[52:55] offset:16384
	s_waitcnt vmcnt(1)
	ds_write_b128 v71, v[56:59] offset:16384
	s_waitcnt vmcnt(0)
	ds_write_b128 v225, v[60:63] offset:57344
	v_mfma_f32_32x32x16_bf16 v[16:31], v[0:3], v[170:173], v[16:31]
	v_add_u32_e32 v221, s0, v220
	v_cmp_gt_u32_e64 s[0:1], 32, v72
	s_waitcnt lgkmcnt(0)
	s_barrier
; #define SWRITE(s) do { *(bf16x8*)(V_lds + (s) * SHM_V + vst0) = vs0; *(bf16x8*)(V_lds + (s) * SHM_V + vst1) = vs1; *(bf16x8*)(K_lds + (s) * SHM_K64 + kst) = ks; } while (0)
; #define ROT() do { s_prev = s_cur; s_cur = s_next; s_next = (s_next == DA_NBUF - 1) ? 0 : s_next + 1; } while (0)
; #define EX2(x) x = __builtin_amdgcn_exp2f(x)
; __device__ __forceinline__ void diff_pass(const bf16_t* __restrict__ Qb, const bf16_t* __restrict__ Kh, const bf16_t* __restrict__ Vh, int seq, char* lds, f32x16 (&o)[4], const int wave_) {
;     ...
;     negm = f32x16{};
;     qkt64c(pA0, pA1, K_lds, qr, negm, r32, hi);
;     { const float pm = rowmax32(pA0, pA1); m_reg = pm; alA = 1.f;
; #pragma unroll
;       for (int r = 0; r < 16; ++r) { pA0[r] -= pm; pA1[r] -= pm; negm[r] = -pm; }
; #pragma unroll
;       for (int r = 0; r < 16; ++r) EX2(pA0[r]);
; #pragma unroll
;       for (int r = 0; r < 8; ++r) EX2(pA1[r]); }
;     SWRITE(1); __syncthreads();
;     ROT();
	v_mfma_f32_32x32x16_bf16 v[32:47], v[4:7], v[174:177], v[32:47]
	v_mov_b64_e32 v[0:1], s[12:13]
	v_mov_b64_e32 v[14:15], s[26:27]
	v_mov_b64_e32 v[2:3], s[14:15]
	v_mov_b64_e32 v[4:5], s[16:17]
	v_mov_b64_e32 v[6:7], s[18:19]
	v_mov_b64_e32 v[8:9], s[20:21]
	v_mov_b64_e32 v[10:11], s[22:23]
	v_mfma_f32_32x32x16_bf16 v[16:31], v[64:67], v[174:177], v[16:31]
	s_nop 3
	v_max_f32_e32 v64, v33, v33
	v_max_f32_e32 v65, v32, v32
	v_max_f32_e32 v64, v65, v64
	v_mov_b64_e32 v[12:13], s[24:25]
	s_nop 3
	v_max3_f32 v65, v34, v35, v17
	v_max3_f32 v64, v64, v16, v18
	v_max3_f32 v64, v64, v19, v36
	v_max3_f32 v65, v65, v38, v39
	v_max3_f32 v64, v64, v37, v20
	v_max3_f32 v65, v65, v22, v23
	v_max3_f32 v64, v64, v21, v40
	v_max3_f32 v65, v65, v42, v43
	v_max3_f32 v64, v64, v41, v24
	v_max3_f32 v65, v65, v26, v27
	v_max3_f32 v64, v64, v25, v44
	v_max3_f32 v65, v65, v46, v47
	v_max3_f32 v64, v64, v45, v28
	v_max3_f32 v65, v65, v30, v31
	v_max3_f32 v64, v64, v29, v65
	v_mov_b32_e32 v65, v64
	s_nop 1
	v_permlane32_swap_b32_e32 v64, v65
	v_max_f32_e32 v65, v65, v65
	v_max_f32_e32 v64, v64, v64
	v_max_f32_e32 v196, v64, v65
	v_sub_f32_e32 v18, v18, v196
	v_sub_f32_e32 v16, v16, v196
	v_sub_f32_e32 v17, v17, v196
	v_sub_f32_e32 v19, v19, v196
	v_exp_f32_e32 v114, v18
	v_and_b32_e32 v18, 7, v68
	v_exp_f32_e32 v112, v16
	v_exp_f32_e32 v113, v17
	v_exp_f32_e32 v115, v19
	v_lshl_add_u64 v[16:17], s[10:11], 0, v[50:51]
	v_lshlrev_b32_e32 v18, 4, v18
	v_mov_b32_e32 v19, v161
	v_sub_f32_e32 v32, v32, v196
	v_sub_f32_e32 v33, v33, v196
	v_sub_f32_e32 v34, v34, v196
	v_sub_f32_e32 v35, v35, v196
	v_sub_f32_e32 v36, v36, v196
	v_sub_f32_e32 v20, v20, v196
	v_sub_f32_e32 v37, v37, v196
	v_sub_f32_e32 v21, v21, v196
	v_sub_f32_e32 v38, v38, v196
	v_sub_f32_e32 v22, v22, v196
	v_sub_f32_e32 v39, v39, v196
	v_sub_f32_e32 v23, v23, v196
	v_sub_f32_e32 v40, v40, v196
	v_sub_f32_e32 v41, v41, v196
	v_pk_add_f32 v[120:121], v[24:25], v[196:197] op_sel_hi:[1,0] neg_lo:[0,1] neg_hi:[0,1]
	v_sub_f32_e32 v24, v42, v196
	v_sub_f32_e32 v25, v43, v196
	v_pk_add_f32 v[122:123], v[26:27], v[196:197] op_sel_hi:[1,0] neg_lo:[0,1] neg_hi:[0,1]
	v_sub_f32_e32 v26, v44, v196
	v_sub_f32_e32 v27, v45, v196
	v_pk_add_f32 v[124:125], v[28:29], v[196:197] op_sel_hi:[1,0] neg_lo:[0,1] neg_hi:[0,1]
	v_sub_f32_e32 v28, v46, v196
	v_sub_f32_e32 v29, v47, v196
	v_lshl_add_u64 v[16:17], v[16:17], 0, v[18:19]
	v_and_b32_e32 v18, 15, v68
	v_exp_f32_e32 v96, v32
	v_exp_f32_e32 v97, v33
	v_exp_f32_e32 v98, v34
	v_exp_f32_e32 v99, v35
	v_exp_f32_e32 v100, v36
	v_exp_f32_e32 v101, v37
	v_exp_f32_e32 v102, v38
	v_exp_f32_e32 v103, v39
	v_exp_f32_e32 v104, v40
	v_exp_f32_e32 v105, v41
	v_exp_f32_e32 v106, v24
	v_exp_f32_e32 v107, v25
	v_exp_f32_e32 v108, v26
	v_exp_f32_e32 v109, v27
	v_exp_f32_e32 v110, v28
	v_exp_f32_e32 v111, v29
	v_exp_f32_e32 v116, v20
	v_exp_f32_e32 v117, v21
	v_exp_f32_e32 v118, v22
	v_exp_f32_e32 v119, v23
	v_lshl_add_u64 v[198:199], s[52:53], 0, v[16:17]
	v_lshl_add_u64 v[16:17], s[10:11], 0, v[48:49]
	v_lshlrev_b32_e32 v18, 4, v18
	v_lshl_add_u64 v[16:17], v[16:17], 0, v[18:19]
	v_xor_b32_e32 v80, 0x80000000, v196
	v_pk_add_f32 v[126:127], v[30:31], v[196:197] op_sel_hi:[1,0] neg_lo:[0,1] neg_hi:[0,1]
	v_lshl_add_u64 v[200:201], s[52:53], 0, v[16:17]
	s_add_u32 s14, s52, s10
	s_addc_u32 s15, s53, s11
	s_add_u32 s14, s14, s64
	s_addc_u32 s15, s15, s65
	s_add_u32 s16, s14, 0x8a40000
	s_addc_u32 s17, s15, 0
	s_add_u32 s14, s14, 0x6a40000
	s_addc_u32 s15, s15, 0
	v_lshrrev_b32_e32 v194, 3, v207
	v_and_b32_e32 v195, 7, v207
	v_lshlrev_b32_e32 v194, 11, v194
	v_lshl_or_b32 v194, v195, 4, v194
	v_lshrrev_b32_e32 v195, 4, v207
	v_and_b32_e32 v255, 15, v207
	v_lshlrev_b32_e32 v195, 11, v195
	v_lshl_or_b32 v195, v255, 4, v195
	v_add_u32_e32 v255, 0x10000, v195
	v_mov_b64_e32 v[62:63], v[14:15]
	v_mov_b64_e32 v[46:47], v[14:15]
	v_mov_b64_e32 v[30:31], v[14:15]
	v_mov_b64_e32 v[60:61], v[12:13]
	v_mov_b64_e32 v[58:59], v[10:11]
	v_mov_b64_e32 v[56:57], v[8:9]
	v_mov_b64_e32 v[54:55], v[6:7]
	v_mov_b64_e32 v[52:53], v[4:5]
	v_mov_b64_e32 v[50:51], v[2:3]
	v_mov_b64_e32 v[48:49], v[0:1]
	v_mov_b64_e32 v[44:45], v[12:13]
	v_mov_b64_e32 v[42:43], v[10:11]
	v_mov_b64_e32 v[40:41], v[8:9]
	v_mov_b64_e32 v[38:39], v[6:7]
	v_mov_b64_e32 v[36:37], v[4:5]
	v_mov_b64_e32 v[34:35], v[2:3]
	v_mov_b64_e32 v[32:33], v[0:1]
	v_mov_b64_e32 v[28:29], v[12:13]
	v_mov_b64_e32 v[26:27], v[10:11]
	v_mov_b64_e32 v[24:25], v[8:9]
	v_mov_b64_e32 v[22:23], v[6:7]
	v_mov_b64_e32 v[20:21], v[4:5]
	v_mov_b64_e32 v[18:19], v[2:3]
	v_mov_b64_e32 v[16:17], v[0:1]
	v_mov_b32_e32 v81, v80
	v_mov_b32_e32 v82, v80
	v_mov_b32_e32 v83, v80
	v_mov_b32_e32 v84, v80
	v_mov_b32_e32 v85, v80
	v_mov_b32_e32 v86, v80
	v_mov_b32_e32 v87, v80
	v_mov_b32_e32 v88, v80
	v_mov_b32_e32 v89, v80
	v_mov_b32_e32 v90, v80
	v_mov_b32_e32 v91, v80
	v_mov_b32_e32 v92, v80
	v_mov_b32_e32 v93, v80
	v_mov_b32_e32 v94, v80
	v_mov_b32_e32 v95, v80

; #define SBAR() __builtin_amdgcn_sched_barrier(0)
; #define SLOAD(k0) do { vs0 = *reinterpret_cast<const bf16x8*>(&Vh[(size_t)((k0) + sr) * DM + sc]); vs1 = *reinterpret_cast<const bf16x8*>(&Vh[(size_t)((k0) + 32 + sr) * DM + sc]); \
;     ks = *reinterpret_cast<const bf16x8*>(&Kh[(size_t)((k0) + kr) * DM + kc]); } while (0)
; __device__ __forceinline__ void diff_pass(const bf16_t* __restrict__ Qb, const bf16_t* __restrict__ Kh, const bf16_t* __restrict__ Vh, int seq, char* lds, f32x16 (&o)[4], const int wave_) {
;     ...
;     for (int j = 1; j + 1 < NT; j += 2) {
;         SLOAD((j + 1) * 64);
;         SBAR(); qkt64c(pB0, pB1, K_lds + s_cur * SHM_K64, qr, negm, r32, hi); FIN(pA0, pA1, alA); SBAR();
;         YSEG(pB0, pB1, alB, s_prev);
.Latt9_p2_top:
	ds_read_b128 v[144:147], v128 offset:49152
	ds_read_b128 v[148:151], v129 offset:49152
	ds_read_b128 v[152:155], v130 offset:49152
	ds_read_b128 v[156:159], v131 offset:49152
	ds_read_b128 v[190:193], v128 offset:53248
	ds_read_b128 v[236:239], v129 offset:53248
	ds_read_b128 v[240:243], v130 offset:53248
	ds_read_b128 v[244:247], v131 offset:53248
	global_load_dwordx4 v[178:181], v195, s[16:17]
	global_load_dwordx4 v[182:185], v255, s[16:17]
	global_load_dwordx4 v[186:189], v194, s[14:15] offset:128
	s_add_u32 s16, s16, 0x20000
	s_addc_u32 s17, s17, 0
	s_add_u32 s14, s14, 0x20000
	s_addc_u32 s15, s15, 0
	v_exp_f32_e32 v208, v120
	v_exp_f32_e32 v209, v121
	v_add_f32_e32 v120, v96, v97
	v_add_f32_e32 v121, v98, v99
	s_waitcnt lgkmcnt(7)
	v_mfma_f32_32x32x16_bf16 v[128:143], v[144:147], v[162:165], v[80:95]
	v_exp_f32_e32 v210, v122
	v_add_f32_e32 v120, v120, v121
	v_add_f32_e32 v121, v100, v101
	v_add_f32_e32 v122, v102, v103
	v_exp_f32_e32 v211, v123
	s_waitcnt lgkmcnt(6)
	v_mfma_f32_32x32x16_bf16 v[128:143], v[148:151], v[166:169], v[128:143]
	v_add_f32_e32 v121, v121, v122
	v_add_f32_e32 v122, v104, v105
	v_add_f32_e32 v123, v106, v107
	v_add_f32_e32 v122, v122, v123
	v_add_f32_e32 v123, v108, v109
	s_waitcnt lgkmcnt(5)
	v_mfma_f32_32x32x16_bf16 v[128:143], v[152:155], v[170:173], v[128:143]
	v_exp_f32_e32 v124, v124
	v_exp_f32_e32 v125, v125
	v_exp_f32_e32 v126, v126
	v_exp_f32_e32 v127, v127
	v_cvt_pk_bf16_f32 v96, v96, v97
	s_waitcnt lgkmcnt(4)
	v_mfma_f32_32x32x16_bf16 v[128:143], v[156:159], v[174:177], v[128:143]
	v_cvt_pk_bf16_f32 v97, v98, v99
	v_cvt_pk_bf16_f32 v98, v100, v101
	v_cvt_pk_bf16_f32 v99, v102, v103
	s_nop 0
	v_permlane32_swap_b32_e32 v96, v98
	s_waitcnt lgkmcnt(3)
	v_mfma_f32_32x32x16_bf16 v[144:159], v[190:193], v[162:165], v[80:95]
	v_add_f32_e32 v190, v110, v111
	v_add_f32_e32 v123, v123, v190
	v_add_f32_e32 v190, v112, v113
	v_add_f32_e32 v191, v114, v115
	v_add_f32_e32 v190, v190, v191
	v_add_f32_e32 v120, v190, v120
	v_add_f32_e32 v190, v116, v117
	s_waitcnt lgkmcnt(2)
	v_mfma_f32_32x32x16_bf16 v[144:159], v[236:239], v[166:169], v[144:159]
	v_lshl_add_u32 v238, s12, 14, v221
	ds_read_b64_tr_b16 v[64:65], v238 offset:0
	ds_read_b64_tr_b16 v[66:67], v238 offset:0x800
	ds_read_b64_tr_b16 v[68:69], v238 offset:0x1000
	ds_read_b64_tr_b16 v[70:71], v238 offset:0x1800
	ds_read_b64_tr_b16 v[72:73], v238 offset:0x2000
	ds_read_b64_tr_b16 v[74:75], v238 offset:0x2800
	ds_read_b64_tr_b16 v[76:77], v238 offset:0x3000
	ds_read_b64_tr_b16 v[78:79], v238 offset:0x3800
	v_add_f32_e32 v191, v118, v119
	v_add_f32_e32 v190, v190, v191
	v_add_f32_e32 v121, v190, v121
	v_add_f32_e32 v190, v208, v209
	v_add_f32_e32 v191, v210, v211
	v_add_f32_e32 v190, v190, v191
	v_add_f32_e32 v122, v122, v190
	s_waitcnt lgkmcnt(9)
	v_mfma_f32_32x32x16_bf16 v[144:159], v[240:243], v[170:173], v[144:159]
	v_add_f32_e32 v190, v124, v125
	v_add_f32_e32 v191, v126, v127
	v_add_f32_e32 v190, v190, v191
	v_add_f32_e32 v123, v123, v190
	v_add_f32_e32 v120, v120, v121
	v_add_f32_e32 v121, v122, v123
	v_add_f32_e32 v235, v120, v121
	s_waitcnt lgkmcnt(8)
	v_mfma_f32_32x32x16_bf16 v[144:159], v[244:247], v[174:177], v[144:159]
	v_mov_b32_e32 v236, v235
	v_cvt_pk_bf16_f32 v120, v104, v105
	v_cvt_pk_bf16_f32 v121, v106, v107
	v_cvt_pk_bf16_f32 v122, v108, v109
	v_cvt_pk_bf16_f32 v123, v110, v111
	v_permlane32_swap_b32_e32 v97, v99
	v_cvt_pk_bf16_f32 v104, v112, v113
	v_cvt_pk_bf16_f32 v105, v114, v115
	v_cvt_pk_bf16_f32 v106, v116, v117
	v_cvt_pk_bf16_f32 v107, v118, v119
	s_waitcnt lgkmcnt(0)
	v_mfma_f32_32x32x16_bf16 v[0:15], v[96:99], v[64:67], v[0:15]
	v_permlane32_swap_b32_e32 v120, v122
	v_permlane32_swap_b32_e32 v121, v123
	v_cvt_pk_bf16_f32 v100, v208, v209
	v_cvt_pk_bf16_f32 v101, v210, v211
	v_cvt_pk_bf16_f32 v102, v124, v125
	v_cvt_pk_bf16_f32 v103, v126, v127
	v_mfma_f32_32x32x16_bf16 v[0:15], v[120:123], v[68:71], v[0:15]
	v_permlane32_swap_b32_e32 v104, v106
	v_permlane32_swap_b32_e32 v105, v107
	ds_read_b64_tr_b16 v[190:191], v238 offset:0x200
	ds_read_b64_tr_b16 v[192:193], v238 offset:0xa00
	ds_read_b64_tr_b16 v[240:241], v238 offset:0x1200
	ds_read_b64_tr_b16 v[242:243], v238 offset:0x1a00
	ds_read_b64_tr_b16 v[244:245], v238 offset:0x2200
	ds_read_b64_tr_b16 v[246:247], v238 offset:0x2a00
	ds_read_b64_tr_b16 v[208:209], v238 offset:0x3200
	ds_read_b64_tr_b16 v[210:211], v238 offset:0x3a00
	v_mfma_f32_32x32x16_bf16 v[0:15], v[104:107], v[72:75], v[0:15]
	v_permlane32_swap_b32_e32 v100, v102
	v_permlane32_swap_b32_e32 v101, v103
	v_permlane32_swap_b32_e32 v235, v236
	v_max_f32_e32 v108, v128, v129
	v_max3_f32 v108, v108, v144, v146
	v_max3_f32 v109, v130, v131, v145
	v_max3_f32 v108, v108, v147, v132
	v_max3_f32 v109, v109, v134, v135
	v_mfma_f32_32x32x16_bf16 v[0:15], v[100:103], v[76:79], v[0:15]
	v_max3_f32 v237, v108, v133, v148
	v_max3_f32 v239, v109, v150, v151
	ds_read_b64_tr_b16 v[124:125], v238 offset:0x400
	ds_read_b64_tr_b16 v[126:127], v238 offset:0xc00
	ds_read_b64_tr_b16 v[116:117], v238 offset:0x1400
	ds_read_b64_tr_b16 v[118:119], v238 offset:0x1c00
	ds_read_b64_tr_b16 v[112:113], v238 offset:0x2400
	ds_read_b64_tr_b16 v[114:115], v238 offset:0x2c00
	ds_read_b64_tr_b16 v[108:109], v238 offset:0x3400
	ds_read_b64_tr_b16 v[110:111], v238 offset:0x3c00
	s_waitcnt lgkmcnt(8)
	v_mfma_f32_32x32x16_bf16 v[48:63], v[96:99], v[190:193], v[48:63]
	v_max3_f32 v190, v237, v149, v136
	v_max3_f32 v191, v239, v138, v139
	v_max3_f32 v190, v190, v137, v152
	v_max3_f32 v191, v191, v154, v155
	v_max3_f32 v190, v190, v153, v140
	v_max3_f32 v191, v191, v142, v143
	v_max3_f32 v190, v190, v141, v156
	v_mfma_f32_32x32x16_bf16 v[48:63], v[120:123], v[240:243], v[48:63]
	v_max3_f32 v191, v191, v158, v159
	v_max3_f32 v190, v190, v157, v191
	v_mov_b32_e32 v191, v190
	s_nop 1
	v_permlane32_swap_b32_e32 v190, v191
	v_mfma_f32_32x32x16_bf16 v[48:63], v[104:107], v[244:247], v[48:63]
	v_max_f32_e32 v237, v190, v191
	s_mov_b32 s2, 0x4138aa3b
	v_cmp_ge_f32_e32 vcc, s2, v237
	v_mfma_f32_32x32x16_bf16 v[48:63], v[100:103], v[208:211], v[48:63]
	s_cmp_eq_u64 vcc, exec
	s_cbranch_scc0 .LBB0_859
	v_mov_b32_e32 v237, 1.0

; #define SBAR() __builtin_amdgcn_sched_barrier(0)
; #define SLOAD(k0) do { vs0 = *reinterpret_cast<const bf16x8*>(&Vh[(size_t)((k0) + sr) * DM + sc]); vs1 = *reinterpret_cast<const bf16x8*>(&Vh[(size_t)((k0) + 32 + sr) * DM + sc]); \
;     ks = *reinterpret_cast<const bf16x8*>(&Kh[(size_t)((k0) + kr) * DM + kc]); } while (0)
; __device__ __forceinline__ void diff_pass(const bf16_t* __restrict__ Qb, const bf16_t* __restrict__ Kh, const bf16_t* __restrict__ Vh, int seq, char* lds, f32x16 (&o)[4], const int wave_) {
;     ...
;         SLOAD((j + 2) * 64);
;         SBAR(); qkt64c(pA0, pA1, K_lds + s_cur * SHM_K64, qr, negm, r32, hi); FIN(pB0, pB1, alB); SBAR();
;         YSEG(pA0, pA1, alA, s_prev);
.LBB0_852:
	s_waitcnt lgkmcnt(0)
	v_add_u32_e32 v102, s2, v227
	v_add_u32_e32 v103, s2, v231
	v_add_u32_e32 v104, s2, v232
	v_add_u32_e32 v105, s2, v233
	s_barrier
	ds_read_b128 v[112:115], v102 offset:49152
	ds_read_b128 v[116:119], v103 offset:49152
	ds_read_b128 v[120:123], v104 offset:49152
	ds_read_b128 v[124:127], v105 offset:49152
	ds_read_b128 v[190:193], v102 offset:53248
	ds_read_b128 v[202:205], v103 offset:53248
	ds_read_b128 v[208:211], v104 offset:53248
	ds_read_b128 v[238:241], v105 offset:53248
	global_load_dwordx4 v[178:181], v195, s[16:17]
	global_load_dwordx4 v[182:185], v255, s[16:17]
	global_load_dwordx4 v[186:189], v194, s[14:15] offset:128
	s_add_u32 s16, s16, 0x20000
	s_addc_u32 s17, s17, 0
	s_add_u32 s14, s14, 0x20000
	s_addc_u32 s15, s15, 0
	v_exp_f32_e32 v242, v152
	v_exp_f32_e32 v243, v153
	v_add_f32_e32 v152, v128, v129
	v_add_f32_e32 v153, v130, v131
	s_waitcnt lgkmcnt(7)
	v_mfma_f32_32x32x16_bf16 v[96:111], v[112:115], v[162:165], v[80:95]
	v_exp_f32_e32 v244, v154
	v_add_f32_e32 v152, v152, v153
	v_add_f32_e32 v153, v132, v133
	v_add_f32_e32 v154, v134, v135
	v_exp_f32_e32 v245, v155
	s_waitcnt lgkmcnt(6)
	v_mfma_f32_32x32x16_bf16 v[96:111], v[116:119], v[166:169], v[96:111]
	v_add_f32_e32 v153, v153, v154
	v_add_f32_e32 v154, v136, v137
	v_add_f32_e32 v155, v138, v139
	v_add_f32_e32 v154, v154, v155
	v_add_f32_e32 v155, v140, v141
	s_waitcnt lgkmcnt(5)
	v_mfma_f32_32x32x16_bf16 v[96:111], v[120:123], v[170:173], v[96:111]
	v_exp_f32_e32 v156, v156
	v_exp_f32_e32 v157, v157
	v_exp_f32_e32 v158, v158
	v_exp_f32_e32 v159, v159
	s_waitcnt lgkmcnt(4)
	v_mfma_f32_32x32x16_bf16 v[96:111], v[124:127], v[174:177], v[96:111]
	s_waitcnt lgkmcnt(3)
	v_mfma_f32_32x32x16_bf16 v[112:127], v[190:193], v[162:165], v[80:95]
	v_add_f32_e32 v190, v142, v143
	v_add_f32_e32 v155, v155, v190
	v_add_f32_e32 v190, v144, v145
	v_add_f32_e32 v191, v146, v147
	v_add_f32_e32 v190, v190, v191
	v_add_f32_e32 v152, v152, v190
	v_add_f32_e32 v190, v148, v149
	s_waitcnt lgkmcnt(2)
	v_mfma_f32_32x32x16_bf16 v[112:127], v[202:205], v[166:169], v[112:127]
	v_lshl_add_u32 v205, s30, 14, v221
	ds_read_b64_tr_b16 v[64:65], v205 offset:0
	ds_read_b64_tr_b16 v[66:67], v205 offset:0x800
	ds_read_b64_tr_b16 v[68:69], v205 offset:0x1000
	ds_read_b64_tr_b16 v[70:71], v205 offset:0x1800
	ds_read_b64_tr_b16 v[72:73], v205 offset:0x2000
	ds_read_b64_tr_b16 v[74:75], v205 offset:0x2800
	ds_read_b64_tr_b16 v[76:77], v205 offset:0x3000
	ds_read_b64_tr_b16 v[78:79], v205 offset:0x3800
	v_add_f32_e32 v191, v150, v151
	v_add_f32_e32 v190, v190, v191
	v_add_f32_e32 v153, v153, v190
	v_add_f32_e32 v190, v242, v243
	v_add_f32_e32 v191, v244, v245
	v_add_f32_e32 v190, v190, v191
	v_add_f32_e32 v154, v154, v190
	s_waitcnt lgkmcnt(9)
	v_mfma_f32_32x32x16_bf16 v[112:127], v[208:211], v[170:173], v[112:127]
	v_add_f32_e32 v190, v156, v157
	v_add_f32_e32 v191, v158, v159
	v_add_f32_e32 v190, v190, v191
	v_add_f32_e32 v155, v155, v190
	v_add_f32_e32 v152, v152, v153
	v_add_f32_e32 v153, v154, v155
	v_add_f32_e32 v203, v152, v153
	s_waitcnt lgkmcnt(8)
	v_mfma_f32_32x32x16_bf16 v[112:127], v[238:241], v[174:177], v[112:127]
	v_mov_b32_e32 v204, v203
	v_cvt_pk_bf16_f32 v152, v128, v129
	v_cvt_pk_bf16_f32 v153, v130, v131
	v_cvt_pk_bf16_f32 v154, v132, v133
	v_cvt_pk_bf16_f32 v155, v134, v135
	v_cvt_pk_bf16_f32 v136, v136, v137
	v_cvt_pk_bf16_f32 v137, v138, v139
	v_cvt_pk_bf16_f32 v138, v140, v141
	v_cvt_pk_bf16_f32 v139, v142, v143
	v_permlane32_swap_b32_e32 v152, v154
	v_permlane32_swap_b32_e32 v153, v155
	v_cvt_pk_bf16_f32 v132, v144, v145
	v_cvt_pk_bf16_f32 v133, v146, v147
	v_cvt_pk_bf16_f32 v134, v148, v149
	v_cvt_pk_bf16_f32 v135, v150, v151
	s_waitcnt lgkmcnt(0)
	v_mfma_f32_32x32x16_bf16 v[0:15], v[152:155], v[64:67], v[0:15]
	v_permlane32_swap_b32_e32 v136, v138
	v_permlane32_swap_b32_e32 v137, v139
	v_cvt_pk_bf16_f32 v128, v242, v243
	v_cvt_pk_bf16_f32 v129, v244, v245
	v_cvt_pk_bf16_f32 v130, v156, v157
	v_cvt_pk_bf16_f32 v131, v158, v159
	v_mfma_f32_32x32x16_bf16 v[0:15], v[136:139], v[68:71], v[0:15]
	v_permlane32_swap_b32_e32 v132, v134
	v_permlane32_swap_b32_e32 v133, v135
	ds_read_b64_tr_b16 v[190:191], v205 offset:0x200
	ds_read_b64_tr_b16 v[192:193], v205 offset:0xa00
	ds_read_b64_tr_b16 v[208:209], v205 offset:0x1200
	ds_read_b64_tr_b16 v[210:211], v205 offset:0x1a00
	ds_read_b64_tr_b16 v[238:239], v205 offset:0x2200
	ds_read_b64_tr_b16 v[240:241], v205 offset:0x2a00
	ds_read_b64_tr_b16 v[242:243], v205 offset:0x3200
	ds_read_b64_tr_b16 v[244:245], v205 offset:0x3a00
	v_mfma_f32_32x32x16_bf16 v[0:15], v[132:135], v[72:75], v[0:15]
	v_permlane32_swap_b32_e32 v128, v130
	v_permlane32_swap_b32_e32 v129, v131
	v_permlane32_swap_b32_e32 v203, v204
	v_max_f32_e32 v140, v96, v97
	v_max3_f32 v140, v140, v112, v114
	v_max3_f32 v141, v98, v99, v113
	v_max3_f32 v140, v140, v115, v100
	v_max3_f32 v141, v141, v102, v103
	v_mfma_f32_32x32x16_bf16 v[0:15], v[128:131], v[76:79], v[0:15]
	v_max3_f32 v202, v140, v101, v116
	v_max3_f32 v246, v141, v118, v119
	ds_read_b64_tr_b16 v[156:157], v205 offset:0x400
	ds_read_b64_tr_b16 v[158:159], v205 offset:0xc00
	ds_read_b64_tr_b16 v[148:149], v205 offset:0x1400
	ds_read_b64_tr_b16 v[150:151], v205 offset:0x1c00
	ds_read_b64_tr_b16 v[144:145], v205 offset:0x2400
	ds_read_b64_tr_b16 v[146:147], v205 offset:0x2c00
	ds_read_b64_tr_b16 v[140:141], v205 offset:0x3400
	ds_read_b64_tr_b16 v[142:143], v205 offset:0x3c00
	s_waitcnt lgkmcnt(8)
	v_mfma_f32_32x32x16_bf16 v[48:63], v[152:155], v[190:193], v[48:63]
	v_max3_f32 v190, v202, v117, v104
	v_max3_f32 v191, v246, v106, v107
	v_max3_f32 v190, v190, v105, v120
	v_max3_f32 v191, v191, v122, v123
	v_max3_f32 v190, v190, v121, v108
	v_max3_f32 v191, v191, v110, v111
	v_max3_f32 v190, v190, v109, v124
	v_mfma_f32_32x32x16_bf16 v[48:63], v[136:139], v[208:211], v[48:63]
	v_max3_f32 v191, v191, v126, v127
	v_max3_f32 v190, v190, v125, v191
	v_mov_b32_e32 v191, v190
	s_nop 1
	v_permlane32_swap_b32_e32 v190, v191
	v_mfma_f32_32x32x16_bf16 v[48:63], v[132:135], v[238:241], v[48:63]
	v_max_f32_e32 v238, v190, v191
	s_mov_b32 s2, 0x4138aa3b
	v_cmp_ge_f32_e32 vcc, s2, v238
	v_mfma_f32_32x32x16_bf16 v[48:63], v[128:131], v[242:245], v[48:63]
	s_cmp_eq_u64 vcc, exec
	v_mov_b32_e32 v202, 1.0
	s_cbranch_scc0 .LBB0_860

; #define SBAR() __builtin_amdgcn_sched_barrier(0)
; #define SLOAD(k0) do { vs0 = *reinterpret_cast<const bf16x8*>(&Vh[(size_t)((k0) + sr) * DM + sc]); vs1 = *reinterpret_cast<const bf16x8*>(&Vh[(size_t)((k0) + 32 + sr) * DM + sc]); \
;     ks = *reinterpret_cast<const bf16x8*>(&Kh[(size_t)((k0) + kr) * DM + kc]); } while (0)
; #define SWRITE(s) do { *(bf16x8*)(V_lds + (s) * SHM_V + vst0) = vs0; *(bf16x8*)(V_lds + (s) * SHM_V + vst1) = vs1; *(bf16x8*)(K_lds + (s) * SHM_K64 + kst) = ks; } while (0)
; #define RESC(a) do { if (__any((a) < 1.f)) { if (hi == 0) al_l[r32] = (a); asm volatile("s_waitcnt lgkmcnt(0)" ::: "memory"); \
;     _Pragma("unroll") for (int d = 0; d < 4; ++d) _Pragma("unroll") for (int r = 0; r < 16; ++r) o[d][r] *= al_l[crow(r, hi)]; } } while (0)
; #define ROT() do { s_prev = s_cur; s_cur = s_next; s_next = (s_next == DA_NBUF - 1) ? 0 : s_next + 1; } while (0)
; __device__ __forceinline__ void diff_pass(const bf16_t* __restrict__ Qb, const bf16_t* __restrict__ Kh, const bf16_t* __restrict__ Vh, int seq, char* lds, f32x16 (&o)[4], const int wave_) {
;     ...
;         SWRITE(s_next); RESC(alB); __syncthreads(); ROT();
;         SLOAD((j + 2) * 64);
;         SBAR(); qkt64c(pA0, pA1, K_lds + s_cur * SHM_K64, qr, negm, r32, hi); FIN(pB0, pB1, alB); SBAR();
;         YSEG(pA0, pA1, alA, s_prev);
;         SWRITE(s_next); RESC(alA); __syncthreads(); ROT();
;     }
.LBB0_857:
	s_add_i32 s2, s30, 1
	v_add_f32_e32 v128, v235, v236
	s_cmp_lg_u32 s30, 2
	v_fmac_f32_e32 v128, v219, v234
	v_add_f32_e32 v219, v203, v204
	s_cselect_b32 s2, s2, 0
	s_add_i32 s28, s28, 2
	v_fmac_f32_e32 v219, v128, v237
	s_lshl_b32 s3, s30, 13
	s_cmp_gt_u32 s28, 28
	v_add_u32_e32 v128, s3, v227
	v_add_u32_e32 v129, s3, v231
	v_add_u32_e32 v130, s3, v232
	v_add_u32_e32 v131, s3, v233
	v_mov_b32_e32 v234, v202
	s_mov_b32 s12, s29
	s_mov_b32 s29, s2
	s_waitcnt lgkmcnt(0)
	s_barrier
	s_cbranch_scc1 .LBB0_861
	s_branch .Latt9_p2_top
